# speedup vs baseline: 1.0187x; 1.0077x over previous
.LBB6_12:
	ds_read_b128 v[176:179], v169
	ds_read_b128 v[180:183], v170
	ds_read_b128 v[184:187], v171
	ds_read_b128 v[188:191], v172
	v_add_u32_e32 v174, 0xc000, v152
	v_lshl_add_u64 v[192:193], v[136:137], 0, s[44:45]
	v_add_u32_e32 v175, 0xe000, v152
	v_add_u32_e32 v173, s17, v168
	v_lshl_add_u64 v[232:233], v[192:193], 0, s[30:31]
	s_mov_b32 m0, s72
	v_lshl_add_u64 v[248:249], v[134:135], 0, s[44:45]
	ds_read_b128 v[196:199], v173
	ds_read_b128 v[200:203], v173 offset:1024
	ds_read_b128 v[204:207], v173 offset:2048
	ds_read_b128 v[212:215], v173 offset:3072
	ds_read_b128 v[216:219], v173 offset:4096
	ds_read_b128 v[220:223], v173 offset:5120
	ds_read_b128 v[224:227], v173 offset:6144
	ds_read_b128 v[228:231], v173 offset:7168
	global_load_lds_dwordx4 v[232:233], off
	s_mov_b32 m0, s73
	v_lshl_add_u64 v[232:233], v[248:249], 0, s[30:31]
	global_load_lds_dwordx4 v[232:233], off
	s_waitcnt lgkmcnt(8)
	s_barrier
	s_waitcnt lgkmcnt(0)
	v_mfma_f32_16x16x32_f16 v[2:5], v[196:199], v[176:179], v[2:5]
	v_mfma_f32_16x16x32_f16 v[6:9], v[196:199], v[184:187], v[6:9]
	v_mfma_f32_16x16x32_f16 v[10:13], v[204:207], v[176:179], v[10:13]
	v_mfma_f32_16x16x32_f16 v[18:21], v[204:207], v[184:187], v[18:21]
	v_mfma_f32_16x16x32_f16 v[30:33], v[216:219], v[176:179], v[30:33]
	v_mfma_f32_16x16x32_f16 v[42:45], v[216:219], v[184:187], v[42:45]
	v_mfma_f32_16x16x32_f16 v[54:57], v[224:227], v[176:179], v[54:57]
	v_mfma_f32_16x16x32_f16 v[66:69], v[224:227], v[184:187], v[66:69]
	v_mfma_f32_16x16x32_f16 v[2:5], v[200:203], v[180:183], v[2:5]
	v_mfma_f32_16x16x32_f16 v[6:9], v[200:203], v[188:191], v[6:9]
	v_mfma_f32_16x16x32_f16 v[10:13], v[212:215], v[180:183], v[10:13]
	v_mfma_f32_16x16x32_f16 v[18:21], v[212:215], v[188:191], v[18:21]
	v_mfma_f32_16x16x32_f16 v[30:33], v[220:223], v[180:183], v[30:33]
	v_mfma_f32_16x16x32_f16 v[42:45], v[220:223], v[188:191], v[42:45]
	v_mfma_f32_16x16x32_f16 v[54:57], v[228:231], v[180:183], v[54:57]
	v_mfma_f32_16x16x32_f16 v[66:69], v[228:231], v[188:191], v[66:69]
	s_barrier
	v_lshl_add_u64 v[250:251], v[140:141], 0, s[44:45]
	v_lshl_add_u64 v[252:253], v[250:251], 0, s[34:35]
	s_mov_b32 m0, s74
	ds_read_b128 v[232:235], v161
	ds_read_b128 v[236:239], v162
	ds_read_b128 v[240:243], v163
	ds_read_b128 v[244:247], v164
	global_load_lds_dwordx4 v[252:253], off
	v_lshl_add_u64 v[252:253], v[138:139], 0, s[44:45]
	s_mov_b32 m0, s75
	v_lshl_add_u64 v[254:255], v[252:253], 0, s[34:35]
	global_load_lds_dwordx4 v[254:255], off
	s_barrier
	s_waitcnt lgkmcnt(0)
	v_mfma_f32_16x16x32_f16 v[14:17], v[196:199], v[232:235], v[14:17]
	v_mfma_f32_16x16x32_f16 v[22:25], v[196:199], v[240:243], v[22:25]
	v_mfma_f32_16x16x32_f16 v[34:37], v[204:207], v[232:235], v[34:37]
	v_mfma_f32_16x16x32_f16 v[46:49], v[204:207], v[240:243], v[46:49]
	v_mfma_f32_16x16x32_f16 v[58:61], v[216:219], v[232:235], v[58:61]
	v_mfma_f32_16x16x32_f16 v[70:73], v[216:219], v[240:243], v[70:73]
	v_mfma_f32_16x16x32_f16 v[78:81], v[224:227], v[232:235], v[78:81]
	v_mfma_f32_16x16x32_f16 v[86:89], v[224:227], v[240:243], v[86:89]
	v_mfma_f32_16x16x32_f16 v[14:17], v[200:203], v[236:239], v[14:17]
	v_mfma_f32_16x16x32_f16 v[22:25], v[200:203], v[244:247], v[22:25]
	v_mfma_f32_16x16x32_f16 v[34:37], v[212:215], v[236:239], v[34:37]
	v_mfma_f32_16x16x32_f16 v[46:49], v[212:215], v[244:247], v[46:49]
	v_mfma_f32_16x16x32_f16 v[58:61], v[220:223], v[236:239], v[58:61]
	v_mfma_f32_16x16x32_f16 v[70:73], v[220:223], v[244:247], v[70:73]
	v_mfma_f32_16x16x32_f16 v[78:81], v[228:231], v[236:239], v[78:81]
	v_mfma_f32_16x16x32_f16 v[86:89], v[228:231], v[244:247], v[86:89]
	v_lshl_add_u64 v[254:255], v[192:193], 0, s[34:35]
	s_mov_b32 m0, s76
	s_barrier
	ds_read_b128 v[196:199], v173 offset:16384
	ds_read_b128 v[200:203], v173 offset:17408
	ds_read_b128 v[204:207], v173 offset:18432
	ds_read_b128 v[212:215], v173 offset:19456
	ds_read_b128 v[216:219], v173 offset:20480
	ds_read_b128 v[220:223], v173 offset:21504
	ds_read_b128 v[224:227], v173 offset:22528
	ds_read_b128 v[228:231], v173 offset:23552
	global_load_lds_dwordx4 v[254:255], off
	s_mov_b32 m0, s77
	v_lshl_add_u64 v[254:255], v[248:249], 0, s[34:35]
	global_load_lds_dwordx4 v[254:255], off
	s_barrier
	s_waitcnt lgkmcnt(0)
	v_mfma_f32_16x16x32_f16 v[26:29], v[196:199], v[176:179], v[26:29]
	v_mfma_f32_16x16x32_f16 v[38:41], v[196:199], v[184:187], v[38:41]
	v_mfma_f32_16x16x32_f16 v[50:53], v[204:207], v[176:179], v[50:53]
	v_mfma_f32_16x16x32_f16 v[62:65], v[204:207], v[184:187], v[62:65]
	v_mfma_f32_16x16x32_f16 v[74:77], v[216:219], v[176:179], v[74:77]
	v_mfma_f32_16x16x32_f16 v[82:85], v[216:219], v[184:187], v[82:85]
	v_mfma_f32_16x16x32_f16 v[90:93], v[224:227], v[176:179], v[90:93]
	v_mfma_f32_16x16x32_f16 v[94:97], v[224:227], v[184:187], v[94:97]
	v_mfma_f32_16x16x32_f16 v[26:29], v[200:203], v[180:183], v[26:29]
	v_mfma_f32_16x16x32_f16 v[38:41], v[200:203], v[188:191], v[38:41]
	v_mfma_f32_16x16x32_f16 v[50:53], v[212:215], v[180:183], v[50:53]
	v_mfma_f32_16x16x32_f16 v[62:65], v[212:215], v[188:191], v[62:65]
	v_mfma_f32_16x16x32_f16 v[74:77], v[220:223], v[180:183], v[74:77]
	v_mfma_f32_16x16x32_f16 v[82:85], v[220:223], v[188:191], v[82:85]
	v_mfma_f32_16x16x32_f16 v[90:93], v[228:231], v[180:183], v[90:93]
	v_mfma_f32_16x16x32_f16 v[94:97], v[228:231], v[188:191], v[94:97]
	s_barrier
	v_lshl_add_u64 v[176:177], v[250:251], 0, s[36:37]
	s_mov_b32 m0, s78
	global_load_lds_dwordx4 v[176:177], off
	s_mov_b32 m0, s79
	v_lshl_add_u64 v[176:177], v[252:253], 0, s[36:37]
	global_load_lds_dwordx4 v[176:177], off
	s_waitcnt vmcnt(6)
	s_barrier
	v_mfma_f32_16x16x32_f16 v[98:101], v[196:199], v[232:235], v[98:101]
	v_mfma_f32_16x16x32_f16 v[102:105], v[196:199], v[240:243], v[102:105]
	v_mfma_f32_16x16x32_f16 v[106:109], v[204:207], v[232:235], v[106:109]
	v_mfma_f32_16x16x32_f16 v[110:113], v[204:207], v[240:243], v[110:113]
	v_mfma_f32_16x16x32_f16 v[114:117], v[216:219], v[232:235], v[114:117]
	v_mfma_f32_16x16x32_f16 v[118:121], v[216:219], v[240:243], v[118:121]
	v_mfma_f32_16x16x32_f16 v[122:125], v[224:227], v[232:235], v[122:125]
	v_mfma_f32_16x16x32_f16 v[126:129], v[224:227], v[240:243], v[126:129]
	v_mfma_f32_16x16x32_f16 v[98:101], v[200:203], v[236:239], v[98:101]
	v_mfma_f32_16x16x32_f16 v[102:105], v[200:203], v[244:247], v[102:105]
	v_mfma_f32_16x16x32_f16 v[106:109], v[212:215], v[236:239], v[106:109]
	v_mfma_f32_16x16x32_f16 v[110:113], v[212:215], v[244:247], v[110:113]
	v_mfma_f32_16x16x32_f16 v[114:117], v[220:223], v[236:239], v[114:117]
	v_mfma_f32_16x16x32_f16 v[118:121], v[220:223], v[244:247], v[118:121]
	v_mfma_f32_16x16x32_f16 v[122:125], v[228:231], v[236:239], v[122:125]
	v_mfma_f32_16x16x32_f16 v[126:129], v[228:231], v[244:247], v[126:129]
	s_barrier
	ds_read_b128 v[176:179], v148
	ds_read_b128 v[180:183], v149
	ds_read_b128 v[184:187], v150
	ds_read_b128 v[188:191], v151
	v_lshl_add_u64 v[232:233], v[192:193], 0, s[36:37]
	s_mov_b32 m0, s80
	ds_read_b128 v[196:199], v173 offset:32768
	ds_read_b128 v[200:203], v173 offset:33792
	ds_read_b128 v[204:207], v173 offset:34816
	ds_read_b128 v[212:215], v173 offset:35840
	ds_read_b128 v[216:219], v173 offset:36864
	ds_read_b128 v[220:223], v173 offset:37888
	ds_read_b128 v[224:227], v173 offset:38912
	ds_read_b128 v[228:231], v173 offset:39936
	global_load_lds_dwordx4 v[232:233], off
	s_mov_b32 m0, s81
	v_lshl_add_u64 v[232:233], v[248:249], 0, s[36:37]
	global_load_lds_dwordx4 v[232:233], off
	s_waitcnt lgkmcnt(8)
	s_barrier
	s_waitcnt lgkmcnt(0)
	v_mfma_f32_16x16x32_f16 v[2:5], v[196:199], v[176:179], v[2:5]
	v_mfma_f32_16x16x32_f16 v[6:9], v[196:199], v[184:187], v[6:9]
	v_mfma_f32_16x16x32_f16 v[10:13], v[204:207], v[176:179], v[10:13]
	v_mfma_f32_16x16x32_f16 v[18:21], v[204:207], v[184:187], v[18:21]
	v_mfma_f32_16x16x32_f16 v[30:33], v[216:219], v[176:179], v[30:33]
	v_mfma_f32_16x16x32_f16 v[42:45], v[216:219], v[184:187], v[42:45]
	v_mfma_f32_16x16x32_f16 v[54:57], v[224:227], v[176:179], v[54:57]
	v_mfma_f32_16x16x32_f16 v[66:69], v[224:227], v[184:187], v[66:69]
	v_mfma_f32_16x16x32_f16 v[2:5], v[200:203], v[180:183], v[2:5]
	v_mfma_f32_16x16x32_f16 v[6:9], v[200:203], v[188:191], v[6:9]
	v_mfma_f32_16x16x32_f16 v[10:13], v[212:215], v[180:183], v[10:13]
	v_mfma_f32_16x16x32_f16 v[18:21], v[212:215], v[188:191], v[18:21]
	v_mfma_f32_16x16x32_f16 v[30:33], v[220:223], v[180:183], v[30:33]
	v_mfma_f32_16x16x32_f16 v[42:45], v[220:223], v[188:191], v[42:45]
	v_mfma_f32_16x16x32_f16 v[54:57], v[228:231], v[180:183], v[54:57]
	v_mfma_f32_16x16x32_f16 v[66:69], v[228:231], v[188:191], v[66:69]
	s_barrier
	v_lshl_add_u64 v[254:255], v[250:251], 0, s[38:39]
	s_mov_b32 m0, s82
	ds_read_b128 v[232:235], v142
	ds_read_b128 v[236:239], v143
	ds_read_b128 v[240:243], v144
	ds_read_b128 v[244:247], v145
	global_load_lds_dwordx4 v[254:255], off
	s_mov_b32 m0, s83
	v_lshl_add_u64 v[254:255], v[252:253], 0, s[38:39]
	global_load_lds_dwordx4 v[254:255], off
	s_barrier
	s_waitcnt lgkmcnt(0)
	v_mfma_f32_16x16x32_f16 v[14:17], v[196:199], v[232:235], v[14:17]
	v_mfma_f32_16x16x32_f16 v[22:25], v[196:199], v[240:243], v[22:25]
	v_mfma_f32_16x16x32_f16 v[34:37], v[204:207], v[232:235], v[34:37]
	v_mfma_f32_16x16x32_f16 v[46:49], v[204:207], v[240:243], v[46:49]
	v_mfma_f32_16x16x32_f16 v[58:61], v[216:219], v[232:235], v[58:61]
	v_mfma_f32_16x16x32_f16 v[70:73], v[216:219], v[240:243], v[70:73]
	v_mfma_f32_16x16x32_f16 v[78:81], v[224:227], v[232:235], v[78:81]
	v_mfma_f32_16x16x32_f16 v[86:89], v[224:227], v[240:243], v[86:89]
	v_mfma_f32_16x16x32_f16 v[14:17], v[200:203], v[236:239], v[14:17]
	v_mfma_f32_16x16x32_f16 v[22:25], v[200:203], v[244:247], v[22:25]
	v_mfma_f32_16x16x32_f16 v[34:37], v[212:215], v[236:239], v[34:37]
	v_mfma_f32_16x16x32_f16 v[46:49], v[212:215], v[244:247], v[46:49]
	v_mfma_f32_16x16x32_f16 v[58:61], v[220:223], v[236:239], v[58:61]
	v_mfma_f32_16x16x32_f16 v[70:73], v[220:223], v[244:247], v[70:73]
	v_mfma_f32_16x16x32_f16 v[78:81], v[228:231], v[236:239], v[78:81]
	v_mfma_f32_16x16x32_f16 v[86:89], v[228:231], v[244:247], v[86:89]
	v_lshl_add_u64 v[192:193], v[192:193], 0, s[38:39]
	s_mov_b32 m0, s84
	s_barrier
	ds_read_b128 v[196:199], v173 offset:49152
	ds_read_b128 v[200:203], v173 offset:50176
	ds_read_b128 v[204:207], v173 offset:51200
	ds_read_b128 v[212:215], v173 offset:52224
	ds_read_b128 v[216:219], v173 offset:53248
	ds_read_b128 v[220:223], v173 offset:54272
	ds_read_b128 v[224:227], v173 offset:55296
	ds_read_b128 v[228:231], v173 offset:56320
	global_load_lds_dwordx4 v[192:193], off
	s_mov_b32 m0, s85
	v_lshl_add_u64 v[192:193], v[248:249], 0, s[38:39]
	global_load_lds_dwordx4 v[192:193], off
	s_barrier
	s_waitcnt lgkmcnt(0)
	v_mfma_f32_16x16x32_f16 v[26:29], v[196:199], v[176:179], v[26:29]
	v_mfma_f32_16x16x32_f16 v[38:41], v[196:199], v[184:187], v[38:41]
	v_mfma_f32_16x16x32_f16 v[50:53], v[204:207], v[176:179], v[50:53]
	v_mfma_f32_16x16x32_f16 v[62:65], v[204:207], v[184:187], v[62:65]
	v_mfma_f32_16x16x32_f16 v[74:77], v[216:219], v[176:179], v[74:77]
	v_mfma_f32_16x16x32_f16 v[82:85], v[216:219], v[184:187], v[82:85]
	v_mfma_f32_16x16x32_f16 v[90:93], v[224:227], v[176:179], v[90:93]
	v_mfma_f32_16x16x32_f16 v[94:97], v[224:227], v[184:187], v[94:97]
	v_mfma_f32_16x16x32_f16 v[26:29], v[200:203], v[180:183], v[26:29]
	v_mfma_f32_16x16x32_f16 v[38:41], v[200:203], v[188:191], v[38:41]
	v_mfma_f32_16x16x32_f16 v[50:53], v[212:215], v[180:183], v[50:53]
	v_mfma_f32_16x16x32_f16 v[62:65], v[212:215], v[188:191], v[62:65]
	v_mfma_f32_16x16x32_f16 v[74:77], v[220:223], v[180:183], v[74:77]
	v_mfma_f32_16x16x32_f16 v[82:85], v[220:223], v[188:191], v[82:85]
	v_mfma_f32_16x16x32_f16 v[90:93], v[228:231], v[180:183], v[90:93]
	v_mfma_f32_16x16x32_f16 v[94:97], v[228:231], v[188:191], v[94:97]
	s_barrier
	v_lshl_add_u64 v[176:177], v[250:251], 0, s[40:41]
	s_mov_b32 m0, s86
	global_load_lds_dwordx4 v[176:177], off
	s_mov_b32 m0, s87
	v_lshl_add_u64 v[176:177], v[252:253], 0, s[40:41]
	global_load_lds_dwordx4 v[176:177], off
	s_waitcnt vmcnt(6)
	s_barrier
	v_mfma_f32_16x16x32_f16 v[98:101], v[196:199], v[232:235], v[98:101]
	v_mfma_f32_16x16x32_f16 v[102:105], v[196:199], v[240:243], v[102:105]
	v_mfma_f32_16x16x32_f16 v[106:109], v[204:207], v[232:235], v[106:109]
	v_mfma_f32_16x16x32_f16 v[110:113], v[204:207], v[240:243], v[110:113]
	v_mfma_f32_16x16x32_f16 v[114:117], v[216:219], v[232:235], v[114:117]
	v_mfma_f32_16x16x32_f16 v[118:121], v[216:219], v[240:243], v[118:121]
	v_mfma_f32_16x16x32_f16 v[122:125], v[224:227], v[232:235], v[122:125]
	v_mfma_f32_16x16x32_f16 v[126:129], v[224:227], v[240:243], v[126:129]
	v_mfma_f32_16x16x32_f16 v[98:101], v[200:203], v[236:239], v[98:101]
	v_mfma_f32_16x16x32_f16 v[102:105], v[200:203], v[244:247], v[102:105]
	v_mfma_f32_16x16x32_f16 v[106:109], v[212:215], v[236:239], v[106:109]
	v_mfma_f32_16x16x32_f16 v[110:113], v[212:215], v[244:247], v[110:113]
	v_mfma_f32_16x16x32_f16 v[114:117], v[220:223], v[236:239], v[114:117]
	v_mfma_f32_16x16x32_f16 v[118:121], v[220:223], v[244:247], v[118:121]
	v_mfma_f32_16x16x32_f16 v[122:125], v[228:231], v[236:239], v[122:125]
	v_mfma_f32_16x16x32_f16 v[126:129], v[228:231], v[244:247], v[126:129]
	s_add_i32 s46, s46, 2
	s_add_u32 s44, s44, 0x100
	s_addc_u32 s45, s45, 0
	s_cmp_lt_u32 s46, 4
	s_barrier
	s_cbranch_scc1 .LBB6_12
	s_add_u32 s0, s0, 0x20380
	s_addc_u32 s1, s1, 0
	v_readfirstlane_b32 s17, v174
	v_lshl_add_u64 v[130:131], v[130:131], 1, s[0:1]
	s_mov_b32 m0, s17
	ds_read_b128 v[134:137], v169
	ds_read_b128 v[138:141], v170
	ds_read_b128 v[152:155], v171
	ds_read_b128 v[156:159], v172
	ds_read_b128 v[166:169], v173
	ds_read_b128 v[176:179], v173 offset:1024
	ds_read_b128 v[180:183], v173 offset:2048
	ds_read_b128 v[184:187], v173 offset:3072
	ds_read_b128 v[188:191], v173 offset:4096
	ds_read_b128 v[196:199], v173 offset:5120
	ds_read_b128 v[200:203], v173 offset:6144
	ds_read_b128 v[204:207], v173 offset:7168
	global_load_lds_dwordx4 v[130:131], off
	v_lshl_add_u64 v[130:131], v[132:133], 1, s[0:1]
	v_readfirstlane_b32 s0, v175
	s_mov_b32 m0, s0
	s_nop 0
	global_load_lds_dwordx4 v[130:131], off
	s_barrier
	s_waitcnt lgkmcnt(0)
	v_mfma_f32_16x16x32_f16 v[2:5], v[166:169], v[134:137], v[2:5]
	v_mfma_f32_16x16x32_f16 v[42:45], v[188:191], v[152:155], v[42:45]
	v_mfma_f32_16x16x32_f16 v[54:57], v[200:203], v[134:137], v[54:57]
	v_mfma_f32_16x16x32_f16 v[66:69], v[200:203], v[152:155], v[66:69]
	v_mfma_f32_16x16x32_f16 v[2:5], v[176:179], v[138:141], v[2:5]
	v_mfma_f32_16x16x32_f16 v[6:9], v[166:169], v[152:155], v[6:9]
	v_mfma_f32_16x16x32_f16 v[10:13], v[180:183], v[134:137], v[10:13]
	v_mfma_f32_16x16x32_f16 v[18:21], v[180:183], v[152:155], v[18:21]
	v_mfma_f32_16x16x32_f16 v[30:33], v[188:191], v[134:137], v[30:33]
	v_mfma_f32_16x16x32_f16 v[42:45], v[196:199], v[156:159], v[42:45]
	v_mfma_f32_16x16x32_f16 v[54:57], v[204:207], v[138:141], v[54:57]
	v_mfma_f32_16x16x32_f16 v[66:69], v[204:207], v[156:159], v[66:69]
	v_mfma_f32_16x16x32_f16 v[6:9], v[176:179], v[156:159], v[6:9]
	v_mfma_f32_16x16x32_f16 v[10:13], v[184:187], v[138:141], v[10:13]
	v_mfma_f32_16x16x32_f16 v[18:21], v[184:187], v[156:159], v[18:21]
	v_mfma_f32_16x16x32_f16 v[30:33], v[196:199], v[138:141], v[30:33]
	s_barrier
	ds_read_b128 v[130:133], v161
	ds_read_b128 v[212:215], v162
	ds_read_b128 v[160:163], v163
	ds_read_b128 v[216:219], v164
	s_barrier
	s_waitcnt lgkmcnt(0)
	v_mfma_f32_16x16x32_f16 v[14:17], v[166:169], v[130:133], v[14:17]
	v_mfma_f32_16x16x32_f16 v[78:81], v[200:203], v[130:133], v[78:81]
	v_mfma_f32_16x16x32_f16 v[14:17], v[176:179], v[212:215], v[14:17]
	v_mfma_f32_16x16x32_f16 v[22:25], v[166:169], v[160:163], v[22:25]
	v_mfma_f32_16x16x32_f16 v[34:37], v[180:183], v[130:133], v[34:37]
	v_mfma_f32_16x16x32_f16 v[46:49], v[180:183], v[160:163], v[46:49]
	v_mfma_f32_16x16x32_f16 v[58:61], v[188:191], v[130:133], v[58:61]
	v_mfma_f32_16x16x32_f16 v[70:73], v[188:191], v[160:163], v[70:73]
	v_mfma_f32_16x16x32_f16 v[164:167], v[204:207], v[212:215], v[78:81]
	v_mfma_f32_16x16x32_f16 v[78:81], v[200:203], v[160:163], v[86:89]
	v_mfma_f32_16x16x32_f16 v[22:25], v[176:179], v[216:219], v[22:25]
	v_mfma_f32_16x16x32_f16 v[34:37], v[184:187], v[212:215], v[34:37]
	v_mfma_f32_16x16x32_f16 v[46:49], v[184:187], v[216:219], v[46:49]
	v_mfma_f32_16x16x32_f16 v[58:61], v[196:199], v[212:215], v[58:61]
	v_mfma_f32_16x16x32_f16 v[70:73], v[196:199], v[216:219], v[70:73]
	v_mfma_f32_16x16x32_f16 v[86:89], v[204:207], v[216:219], v[78:81]
	s_barrier
	s_nop 0
	ds_read_b128 v[78:81], v173 offset:16384
	ds_read_b128 v[168:171], v173 offset:17408
	ds_read_b128 v[174:177], v173 offset:18432
	ds_read_b128 v[178:181], v173 offset:19456
	ds_read_b128 v[182:185], v173 offset:20480
	ds_read_b128 v[186:189], v173 offset:21504
	ds_read_b128 v[190:193], v173 offset:22528
	ds_read_b128 v[196:199], v173 offset:23552
	s_waitcnt vmcnt(4)
	s_barrier
	s_waitcnt lgkmcnt(0)
	v_mfma_f32_16x16x32_f16 v[26:29], v[78:81], v[134:137], v[26:29]
	v_mfma_f32_16x16x32_f16 v[38:41], v[78:81], v[152:155], v[38:41]
	v_mfma_f32_16x16x32_f16 v[26:29], v[168:171], v[138:141], v[26:29]
	v_mfma_f32_16x16x32_f16 v[38:41], v[168:171], v[156:159], v[38:41]
	v_mfma_f32_16x16x32_f16 v[50:53], v[174:177], v[134:137], v[50:53]
	v_mfma_f32_16x16x32_f16 v[62:65], v[174:177], v[152:155], v[62:65]
	v_mfma_f32_16x16x32_f16 v[74:77], v[182:185], v[134:137], v[74:77]
	v_mfma_f32_16x16x32_f16 v[82:85], v[182:185], v[152:155], v[82:85]
	v_mfma_f32_16x16x32_f16 v[90:93], v[190:193], v[134:137], v[90:93]
	v_mfma_f32_16x16x32_f16 v[94:97], v[190:193], v[152:155], v[94:97]
	v_mfma_f32_16x16x32_f16 v[50:53], v[178:181], v[138:141], v[50:53]
	v_mfma_f32_16x16x32_f16 v[62:65], v[178:181], v[156:159], v[62:65]
	v_mfma_f32_16x16x32_f16 v[74:77], v[186:189], v[138:141], v[74:77]
	v_mfma_f32_16x16x32_f16 v[82:85], v[186:189], v[156:159], v[82:85]
	v_mfma_f32_16x16x32_f16 v[90:93], v[196:199], v[138:141], v[90:93]
	v_mfma_f32_16x16x32_f16 v[94:97], v[196:199], v[156:159], v[94:97]
	v_mfma_f32_16x16x32_f16 v[98:101], v[78:81], v[130:133], v[98:101]
	v_mfma_f32_16x16x32_f16 v[78:81], v[78:81], v[160:163], v[102:105]
	v_mfma_f32_16x16x32_f16 v[102:105], v[168:171], v[216:219], v[78:81]
	v_mfma_f32_16x16x32_f16 v[78:81], v[174:177], v[130:133], v[106:109]
	v_mfma_f32_16x16x32_f16 v[106:109], v[178:181], v[212:215], v[78:81]
	v_mfma_f32_16x16x32_f16 v[78:81], v[174:177], v[160:163], v[110:113]
	v_mfma_f32_16x16x32_f16 v[200:203], v[178:181], v[216:219], v[78:81]
	v_mfma_f32_16x16x32_f16 v[78:81], v[182:185], v[130:133], v[114:117]
	v_mfma_f32_16x16x32_f16 v[204:207], v[186:189], v[212:215], v[78:81]
	v_mfma_f32_16x16x32_f16 v[78:81], v[182:185], v[160:163], v[118:121]
	v_mfma_f32_16x16x32_f16 v[220:223], v[186:189], v[216:219], v[78:81]
	v_mfma_f32_16x16x32_f16 v[78:81], v[190:193], v[130:133], v[122:125]
	v_mfma_f32_16x16x32_f16 v[98:101], v[168:171], v[212:215], v[98:101]
	v_mfma_f32_16x16x32_f16 v[212:215], v[196:199], v[212:215], v[78:81]
	v_mfma_f32_16x16x32_f16 v[78:81], v[190:193], v[160:163], v[126:129]
	v_mfma_f32_16x16x32_f16 v[196:199], v[196:199], v[216:219], v[78:81]
	s_barrier
	ds_read_b128 v[110:113], v148
	ds_read_b128 v[130:133], v149
	ds_read_b128 v[216:219], v150
	ds_read_b128 v[224:227], v151
	s_nop 0
	ds_read_b128 v[78:81], v173 offset:32768
	ds_read_b128 v[114:117], v173 offset:33792
	ds_read_b128 v[118:121], v173 offset:34816
	ds_read_b128 v[134:137], v173 offset:35840
	ds_read_b128 v[138:141], v173 offset:36864
	ds_read_b128 v[168:171], v173 offset:37888
	ds_read_b128 v[174:177], v173 offset:38912
	ds_read_b128 v[228:231], v173 offset:39936
	s_waitcnt vmcnt(2)
	s_barrier
	s_waitcnt lgkmcnt(0)
	v_mfma_f32_16x16x32_f16 v[2:5], v[78:81], v[110:113], v[2:5]
	v_mfma_f32_16x16x32_f16 v[190:193], v[114:117], v[130:133], v[2:5]
	v_mfma_f32_16x16x32_f16 v[2:5], v[78:81], v[216:219], v[6:9]
	v_mfma_f32_16x16x32_f16 v[158:161], v[114:117], v[224:227], v[2:5]
	v_mfma_f32_16x16x32_f16 v[2:5], v[118:121], v[110:113], v[10:13]
	v_mfma_f32_16x16x32_f16 v[186:189], v[134:137], v[130:133], v[2:5]
	v_mfma_f32_16x16x32_f16 v[2:5], v[118:121], v[216:219], v[18:21]
	v_mfma_f32_16x16x32_f16 v[154:157], v[134:137], v[224:227], v[2:5]
	v_mfma_f32_16x16x32_f16 v[2:5], v[138:141], v[110:113], v[30:33]
	v_mfma_f32_16x16x32_f16 v[182:185], v[168:171], v[130:133], v[2:5]
	v_mfma_f32_16x16x32_f16 v[2:5], v[138:141], v[216:219], v[42:45]
	v_mfma_f32_16x16x32_f16 v[150:153], v[168:171], v[224:227], v[2:5]
	v_mfma_f32_16x16x32_f16 v[2:5], v[174:177], v[110:113], v[54:57]
	v_mfma_f32_16x16x32_f16 v[178:181], v[228:231], v[130:133], v[2:5]
	v_mfma_f32_16x16x32_f16 v[2:5], v[174:177], v[216:219], v[66:69]
	v_mfma_f32_16x16x32_f16 v[146:149], v[228:231], v[224:227], v[2:5]
	s_barrier
	s_nop 4
	ds_read_b128 v[2:5], v142
	ds_read_b128 v[6:9], v143
	ds_read_b128 v[10:13], v144
	ds_read_b128 v[18:21], v145
	s_waitcnt vmcnt(0)
	s_barrier
	s_waitcnt lgkmcnt(0)
	v_mfma_f32_16x16x32_f16 v[14:17], v[78:81], v[2:5], v[14:17]
	v_mfma_f32_16x16x32_f16 v[126:129], v[114:117], v[6:9], v[14:17]
	v_mfma_f32_16x16x32_f16 v[14:17], v[78:81], v[10:13], v[22:25]
	v_mfma_f32_16x16x32_f16 v[78:81], v[114:117], v[18:21], v[14:17]
	v_mfma_f32_16x16x32_f16 v[14:17], v[118:121], v[2:5], v[34:37]
	v_mfma_f32_16x16x32_f16 v[122:125], v[134:137], v[6:9], v[14:17]
	v_mfma_f32_16x16x32_f16 v[14:17], v[118:121], v[10:13], v[46:49]
	v_mfma_f32_16x16x32_f16 v[66:69], v[134:137], v[18:21], v[14:17]
	v_mfma_f32_16x16x32_f16 v[14:17], v[138:141], v[2:5], v[58:61]
	v_mfma_f32_16x16x32_f16 v[118:121], v[168:171], v[6:9], v[14:17]
	v_mfma_f32_16x16x32_f16 v[14:17], v[138:141], v[10:13], v[70:73]
	v_mfma_f32_16x16x32_f16 v[54:57], v[168:171], v[18:21], v[14:17]
	v_mfma_f32_16x16x32_f16 v[14:17], v[174:177], v[2:5], v[164:167]
	v_mfma_f32_16x16x32_f16 v[114:117], v[228:231], v[6:9], v[14:17]
	v_mfma_f32_16x16x32_f16 v[14:17], v[174:177], v[10:13], v[86:89]
	v_mfma_f32_16x16x32_f16 v[42:45], v[228:231], v[18:21], v[14:17]
	s_barrier
	s_nop 4
	ds_read_b128 v[14:17], v173 offset:49152
	ds_read_b128 v[22:25], v173 offset:50176
	ds_read_b128 v[30:33], v173 offset:51200
	ds_read_b128 v[34:37], v173 offset:52224
	ds_read_b128 v[46:49], v173 offset:53248
	ds_read_b128 v[58:61], v173 offset:54272
	ds_read_b128 v[70:73], v173 offset:55296
	ds_read_b128 v[86:89], v173 offset:56320
	s_barrier
	s_waitcnt lgkmcnt(0)
	v_mfma_f32_16x16x32_f16 v[26:29], v[14:17], v[110:113], v[26:29]
	v_mfma_f32_16x16x32_f16 v[174:177], v[22:25], v[130:133], v[26:29]
	v_mfma_f32_16x16x32_f16 v[26:29], v[14:17], v[216:219], v[38:41]
	v_mfma_f32_16x16x32_f16 v[142:145], v[22:25], v[224:227], v[26:29]
	v_mfma_f32_16x16x32_f16 v[26:29], v[30:33], v[110:113], v[50:53]
	v_mfma_f32_16x16x32_f16 v[170:173], v[34:37], v[130:133], v[26:29]
	v_mfma_f32_16x16x32_f16 v[26:29], v[30:33], v[216:219], v[62:65]
	v_mfma_f32_16x16x32_f16 v[138:141], v[34:37], v[224:227], v[26:29]
	v_mfma_f32_16x16x32_f16 v[26:29], v[46:49], v[110:113], v[74:77]
	v_mfma_f32_16x16x32_f16 v[166:169], v[58:61], v[130:133], v[26:29]
	v_mfma_f32_16x16x32_f16 v[26:29], v[46:49], v[216:219], v[82:85]
	v_mfma_f32_16x16x32_f16 v[134:137], v[58:61], v[224:227], v[26:29]
	v_mfma_f32_16x16x32_f16 v[26:29], v[70:73], v[110:113], v[90:93]
	v_mfma_f32_16x16x32_f16 v[162:165], v[86:89], v[130:133], v[26:29]
	v_mfma_f32_16x16x32_f16 v[26:29], v[70:73], v[216:219], v[94:97]
	v_mfma_f32_16x16x32_f16 v[130:133], v[86:89], v[224:227], v[26:29]
	v_mfma_f32_16x16x32_f16 v[26:29], v[14:17], v[2:5], v[98:101]
	v_mfma_f32_16x16x32_f16 v[14:17], v[14:17], v[10:13], v[102:105]
	v_mfma_f32_16x16x32_f16 v[38:41], v[22:25], v[18:21], v[14:17]
	v_mfma_f32_16x16x32_f16 v[14:17], v[30:33], v[2:5], v[106:109]
	v_mfma_f32_16x16x32_f16 v[106:109], v[34:37], v[6:9], v[14:17]
	v_mfma_f32_16x16x32_f16 v[14:17], v[30:33], v[10:13], v[200:203]
	v_mfma_f32_16x16x32_f16 v[110:113], v[22:25], v[6:9], v[26:29]
	v_mfma_f32_16x16x32_f16 v[26:29], v[34:37], v[18:21], v[14:17]
	v_mfma_f32_16x16x32_f16 v[14:17], v[46:49], v[2:5], v[204:207]
	v_mfma_f32_16x16x32_f16 v[2:5], v[70:73], v[2:5], v[212:215]
	v_mfma_f32_16x16x32_f16 v[102:105], v[58:61], v[6:9], v[14:17]
	v_mfma_f32_16x16x32_f16 v[14:17], v[46:49], v[10:13], v[220:223]
	v_mfma_f32_16x16x32_f16 v[98:101], v[86:89], v[6:9], v[2:5]
	v_mfma_f32_16x16x32_f16 v[2:5], v[70:73], v[10:13], v[196:199]
	v_mfma_f32_16x16x32_f16 v[14:17], v[58:61], v[18:21], v[14:17]
	v_mfma_f32_16x16x32_f16 v[2:5], v[86:89], v[18:21], v[2:5]
	s_cmpk_gt_u32 s65, 0xff
	s_barrier
	s_cbranch_scc1 .LBB6_15
	s_barrier

.LBB7_239:
	ds_read_b128 v[176:179], v169
	ds_read_b128 v[180:183], v170
	ds_read_b128 v[184:187], v171
	ds_read_b128 v[188:191], v172
	v_add_u32_e32 v174, 0xc000, v152
	v_lshl_add_u64 v[192:193], v[136:137], 0, s[46:47]
	v_add_u32_e32 v175, 0xe000, v152
	v_add_u32_e32 v173, s5, v168
	v_lshl_add_u64 v[232:233], v[192:193], 0, s[34:35]
	s_mov_b32 m0, s72
	v_lshl_add_u64 v[248:249], v[134:135], 0, s[46:47]
	ds_read_b128 v[196:199], v173
	ds_read_b128 v[200:203], v173 offset:1024
	ds_read_b128 v[204:207], v173 offset:2048
	ds_read_b128 v[212:215], v173 offset:3072
	ds_read_b128 v[216:219], v173 offset:4096
	ds_read_b128 v[220:223], v173 offset:5120
	ds_read_b128 v[224:227], v173 offset:6144
	ds_read_b128 v[228:231], v173 offset:7168
	global_load_lds_dwordx4 v[232:233], off
	s_mov_b32 m0, s73
	v_lshl_add_u64 v[232:233], v[248:249], 0, s[34:35]
	global_load_lds_dwordx4 v[232:233], off
	s_waitcnt lgkmcnt(8)
	s_barrier
	s_waitcnt lgkmcnt(0)
	v_mfma_f32_16x16x32_f16 v[2:5], v[196:199], v[176:179], v[2:5]
	v_mfma_f32_16x16x32_f16 v[6:9], v[196:199], v[184:187], v[6:9]
	v_mfma_f32_16x16x32_f16 v[10:13], v[204:207], v[176:179], v[10:13]
	v_mfma_f32_16x16x32_f16 v[18:21], v[204:207], v[184:187], v[18:21]
	v_mfma_f32_16x16x32_f16 v[30:33], v[216:219], v[176:179], v[30:33]
	v_mfma_f32_16x16x32_f16 v[42:45], v[216:219], v[184:187], v[42:45]
	v_mfma_f32_16x16x32_f16 v[54:57], v[224:227], v[176:179], v[54:57]
	v_mfma_f32_16x16x32_f16 v[66:69], v[224:227], v[184:187], v[66:69]
	v_mfma_f32_16x16x32_f16 v[2:5], v[200:203], v[180:183], v[2:5]
	v_mfma_f32_16x16x32_f16 v[6:9], v[200:203], v[188:191], v[6:9]
	v_mfma_f32_16x16x32_f16 v[10:13], v[212:215], v[180:183], v[10:13]
	v_mfma_f32_16x16x32_f16 v[18:21], v[212:215], v[188:191], v[18:21]
	v_mfma_f32_16x16x32_f16 v[30:33], v[220:223], v[180:183], v[30:33]
	v_mfma_f32_16x16x32_f16 v[42:45], v[220:223], v[188:191], v[42:45]
	v_mfma_f32_16x16x32_f16 v[54:57], v[228:231], v[180:183], v[54:57]
	v_mfma_f32_16x16x32_f16 v[66:69], v[228:231], v[188:191], v[66:69]
	s_barrier
	v_lshl_add_u64 v[250:251], v[140:141], 0, s[46:47]
	v_lshl_add_u64 v[252:253], v[250:251], 0, s[36:37]
	s_mov_b32 m0, s74
	ds_read_b128 v[232:235], v161
	ds_read_b128 v[236:239], v162
	ds_read_b128 v[240:243], v163
	ds_read_b128 v[244:247], v164
	global_load_lds_dwordx4 v[252:253], off
	v_lshl_add_u64 v[252:253], v[138:139], 0, s[46:47]
	s_mov_b32 m0, s75
	v_lshl_add_u64 v[254:255], v[252:253], 0, s[36:37]
	global_load_lds_dwordx4 v[254:255], off
	s_barrier
	s_waitcnt lgkmcnt(0)
	v_mfma_f32_16x16x32_f16 v[14:17], v[196:199], v[232:235], v[14:17]
	v_mfma_f32_16x16x32_f16 v[22:25], v[196:199], v[240:243], v[22:25]
	v_mfma_f32_16x16x32_f16 v[34:37], v[204:207], v[232:235], v[34:37]
	v_mfma_f32_16x16x32_f16 v[46:49], v[204:207], v[240:243], v[46:49]
	v_mfma_f32_16x16x32_f16 v[58:61], v[216:219], v[232:235], v[58:61]
	v_mfma_f32_16x16x32_f16 v[70:73], v[216:219], v[240:243], v[70:73]
	v_mfma_f32_16x16x32_f16 v[78:81], v[224:227], v[232:235], v[78:81]
	v_mfma_f32_16x16x32_f16 v[86:89], v[224:227], v[240:243], v[86:89]
	v_mfma_f32_16x16x32_f16 v[14:17], v[200:203], v[236:239], v[14:17]
	v_mfma_f32_16x16x32_f16 v[22:25], v[200:203], v[244:247], v[22:25]
	v_mfma_f32_16x16x32_f16 v[34:37], v[212:215], v[236:239], v[34:37]
	v_mfma_f32_16x16x32_f16 v[46:49], v[212:215], v[244:247], v[46:49]
	v_mfma_f32_16x16x32_f16 v[58:61], v[220:223], v[236:239], v[58:61]
	v_mfma_f32_16x16x32_f16 v[70:73], v[220:223], v[244:247], v[70:73]
	v_mfma_f32_16x16x32_f16 v[78:81], v[228:231], v[236:239], v[78:81]
	v_mfma_f32_16x16x32_f16 v[86:89], v[228:231], v[244:247], v[86:89]
	v_lshl_add_u64 v[254:255], v[192:193], 0, s[36:37]
	s_mov_b32 m0, s76
	s_barrier
	ds_read_b128 v[196:199], v173 offset:16384
	ds_read_b128 v[200:203], v173 offset:17408
	ds_read_b128 v[204:207], v173 offset:18432
	ds_read_b128 v[212:215], v173 offset:19456
	ds_read_b128 v[216:219], v173 offset:20480
	ds_read_b128 v[220:223], v173 offset:21504
	ds_read_b128 v[224:227], v173 offset:22528
	ds_read_b128 v[228:231], v173 offset:23552
	global_load_lds_dwordx4 v[254:255], off
	s_mov_b32 m0, s77
	v_lshl_add_u64 v[254:255], v[248:249], 0, s[36:37]
	global_load_lds_dwordx4 v[254:255], off
	s_barrier
	s_waitcnt lgkmcnt(0)
	v_mfma_f32_16x16x32_f16 v[26:29], v[196:199], v[176:179], v[26:29]
	v_mfma_f32_16x16x32_f16 v[38:41], v[196:199], v[184:187], v[38:41]
	v_mfma_f32_16x16x32_f16 v[50:53], v[204:207], v[176:179], v[50:53]
	v_mfma_f32_16x16x32_f16 v[62:65], v[204:207], v[184:187], v[62:65]
	v_mfma_f32_16x16x32_f16 v[74:77], v[216:219], v[176:179], v[74:77]
	v_mfma_f32_16x16x32_f16 v[82:85], v[216:219], v[184:187], v[82:85]
	v_mfma_f32_16x16x32_f16 v[90:93], v[224:227], v[176:179], v[90:93]
	v_mfma_f32_16x16x32_f16 v[94:97], v[224:227], v[184:187], v[94:97]
	v_mfma_f32_16x16x32_f16 v[26:29], v[200:203], v[180:183], v[26:29]
	v_mfma_f32_16x16x32_f16 v[38:41], v[200:203], v[188:191], v[38:41]
	v_mfma_f32_16x16x32_f16 v[50:53], v[212:215], v[180:183], v[50:53]
	v_mfma_f32_16x16x32_f16 v[62:65], v[212:215], v[188:191], v[62:65]
	v_mfma_f32_16x16x32_f16 v[74:77], v[220:223], v[180:183], v[74:77]
	v_mfma_f32_16x16x32_f16 v[82:85], v[220:223], v[188:191], v[82:85]
	v_mfma_f32_16x16x32_f16 v[90:93], v[228:231], v[180:183], v[90:93]
	v_mfma_f32_16x16x32_f16 v[94:97], v[228:231], v[188:191], v[94:97]
	s_barrier
	v_lshl_add_u64 v[176:177], v[250:251], 0, s[38:39]
	s_mov_b32 m0, s78
	global_load_lds_dwordx4 v[176:177], off
	s_mov_b32 m0, s79
	v_lshl_add_u64 v[176:177], v[252:253], 0, s[38:39]
	global_load_lds_dwordx4 v[176:177], off
	s_waitcnt vmcnt(6)
	s_barrier
	v_mfma_f32_16x16x32_f16 v[98:101], v[196:199], v[232:235], v[98:101]
	v_mfma_f32_16x16x32_f16 v[102:105], v[196:199], v[240:243], v[102:105]
	v_mfma_f32_16x16x32_f16 v[106:109], v[204:207], v[232:235], v[106:109]
	v_mfma_f32_16x16x32_f16 v[110:113], v[204:207], v[240:243], v[110:113]
	v_mfma_f32_16x16x32_f16 v[114:117], v[216:219], v[232:235], v[114:117]
	v_mfma_f32_16x16x32_f16 v[118:121], v[216:219], v[240:243], v[118:121]
	v_mfma_f32_16x16x32_f16 v[122:125], v[224:227], v[232:235], v[122:125]
	v_mfma_f32_16x16x32_f16 v[126:129], v[224:227], v[240:243], v[126:129]
	v_mfma_f32_16x16x32_f16 v[98:101], v[200:203], v[236:239], v[98:101]
	v_mfma_f32_16x16x32_f16 v[102:105], v[200:203], v[244:247], v[102:105]
	v_mfma_f32_16x16x32_f16 v[106:109], v[212:215], v[236:239], v[106:109]
	v_mfma_f32_16x16x32_f16 v[110:113], v[212:215], v[244:247], v[110:113]
	v_mfma_f32_16x16x32_f16 v[114:117], v[220:223], v[236:239], v[114:117]
	v_mfma_f32_16x16x32_f16 v[118:121], v[220:223], v[244:247], v[118:121]
	v_mfma_f32_16x16x32_f16 v[122:125], v[228:231], v[236:239], v[122:125]
	v_mfma_f32_16x16x32_f16 v[126:129], v[228:231], v[244:247], v[126:129]
	s_barrier
	ds_read_b128 v[176:179], v148
	ds_read_b128 v[180:183], v149
	ds_read_b128 v[184:187], v150
	ds_read_b128 v[188:191], v151
	v_lshl_add_u64 v[232:233], v[192:193], 0, s[38:39]
	s_mov_b32 m0, s80
	ds_read_b128 v[196:199], v173 offset:32768
	ds_read_b128 v[200:203], v173 offset:33792
	ds_read_b128 v[204:207], v173 offset:34816
	ds_read_b128 v[212:215], v173 offset:35840
	ds_read_b128 v[216:219], v173 offset:36864
	ds_read_b128 v[220:223], v173 offset:37888
	ds_read_b128 v[224:227], v173 offset:38912
	ds_read_b128 v[228:231], v173 offset:39936
	global_load_lds_dwordx4 v[232:233], off
	s_mov_b32 m0, s81
	v_lshl_add_u64 v[232:233], v[248:249], 0, s[38:39]
	global_load_lds_dwordx4 v[232:233], off
	s_waitcnt lgkmcnt(8)
	s_barrier
	s_waitcnt lgkmcnt(0)
	v_mfma_f32_16x16x32_f16 v[2:5], v[196:199], v[176:179], v[2:5]
	v_mfma_f32_16x16x32_f16 v[6:9], v[196:199], v[184:187], v[6:9]
	v_mfma_f32_16x16x32_f16 v[10:13], v[204:207], v[176:179], v[10:13]
	v_mfma_f32_16x16x32_f16 v[18:21], v[204:207], v[184:187], v[18:21]
	v_mfma_f32_16x16x32_f16 v[30:33], v[216:219], v[176:179], v[30:33]
	v_mfma_f32_16x16x32_f16 v[42:45], v[216:219], v[184:187], v[42:45]
	v_mfma_f32_16x16x32_f16 v[54:57], v[224:227], v[176:179], v[54:57]
	v_mfma_f32_16x16x32_f16 v[66:69], v[224:227], v[184:187], v[66:69]
	v_mfma_f32_16x16x32_f16 v[2:5], v[200:203], v[180:183], v[2:5]
	v_mfma_f32_16x16x32_f16 v[6:9], v[200:203], v[188:191], v[6:9]
	v_mfma_f32_16x16x32_f16 v[10:13], v[212:215], v[180:183], v[10:13]
	v_mfma_f32_16x16x32_f16 v[18:21], v[212:215], v[188:191], v[18:21]
	v_mfma_f32_16x16x32_f16 v[30:33], v[220:223], v[180:183], v[30:33]
	v_mfma_f32_16x16x32_f16 v[42:45], v[220:223], v[188:191], v[42:45]
	v_mfma_f32_16x16x32_f16 v[54:57], v[228:231], v[180:183], v[54:57]
	v_mfma_f32_16x16x32_f16 v[66:69], v[228:231], v[188:191], v[66:69]
	s_barrier
	v_lshl_add_u64 v[254:255], v[250:251], 0, s[40:41]
	s_mov_b32 m0, s82
	ds_read_b128 v[232:235], v142
	ds_read_b128 v[236:239], v143
	ds_read_b128 v[240:243], v144
	ds_read_b128 v[244:247], v145
	global_load_lds_dwordx4 v[254:255], off
	s_mov_b32 m0, s83
	v_lshl_add_u64 v[254:255], v[252:253], 0, s[40:41]
	global_load_lds_dwordx4 v[254:255], off
	s_barrier
	s_waitcnt lgkmcnt(0)
	v_mfma_f32_16x16x32_f16 v[14:17], v[196:199], v[232:235], v[14:17]
	v_mfma_f32_16x16x32_f16 v[22:25], v[196:199], v[240:243], v[22:25]
	v_mfma_f32_16x16x32_f16 v[34:37], v[204:207], v[232:235], v[34:37]
	v_mfma_f32_16x16x32_f16 v[46:49], v[204:207], v[240:243], v[46:49]
	v_mfma_f32_16x16x32_f16 v[58:61], v[216:219], v[232:235], v[58:61]
	v_mfma_f32_16x16x32_f16 v[70:73], v[216:219], v[240:243], v[70:73]
	v_mfma_f32_16x16x32_f16 v[78:81], v[224:227], v[232:235], v[78:81]
	v_mfma_f32_16x16x32_f16 v[86:89], v[224:227], v[240:243], v[86:89]
	v_mfma_f32_16x16x32_f16 v[14:17], v[200:203], v[236:239], v[14:17]
	v_mfma_f32_16x16x32_f16 v[22:25], v[200:203], v[244:247], v[22:25]
	v_mfma_f32_16x16x32_f16 v[34:37], v[212:215], v[236:239], v[34:37]
	v_mfma_f32_16x16x32_f16 v[46:49], v[212:215], v[244:247], v[46:49]
	v_mfma_f32_16x16x32_f16 v[58:61], v[220:223], v[236:239], v[58:61]
	v_mfma_f32_16x16x32_f16 v[70:73], v[220:223], v[244:247], v[70:73]
	v_mfma_f32_16x16x32_f16 v[78:81], v[228:231], v[236:239], v[78:81]
	v_mfma_f32_16x16x32_f16 v[86:89], v[228:231], v[244:247], v[86:89]
	v_lshl_add_u64 v[192:193], v[192:193], 0, s[40:41]
	s_mov_b32 m0, s84
	s_barrier
	ds_read_b128 v[196:199], v173 offset:49152
	ds_read_b128 v[200:203], v173 offset:50176
	ds_read_b128 v[204:207], v173 offset:51200
	ds_read_b128 v[212:215], v173 offset:52224
	ds_read_b128 v[216:219], v173 offset:53248
	ds_read_b128 v[220:223], v173 offset:54272
	ds_read_b128 v[224:227], v173 offset:55296
	ds_read_b128 v[228:231], v173 offset:56320
	global_load_lds_dwordx4 v[192:193], off
	s_mov_b32 m0, s85
	v_lshl_add_u64 v[192:193], v[248:249], 0, s[40:41]
	global_load_lds_dwordx4 v[192:193], off
	s_barrier
	s_waitcnt lgkmcnt(0)
	v_mfma_f32_16x16x32_f16 v[26:29], v[196:199], v[176:179], v[26:29]
	v_mfma_f32_16x16x32_f16 v[38:41], v[196:199], v[184:187], v[38:41]
	v_mfma_f32_16x16x32_f16 v[50:53], v[204:207], v[176:179], v[50:53]
	v_mfma_f32_16x16x32_f16 v[62:65], v[204:207], v[184:187], v[62:65]
	v_mfma_f32_16x16x32_f16 v[74:77], v[216:219], v[176:179], v[74:77]
	v_mfma_f32_16x16x32_f16 v[82:85], v[216:219], v[184:187], v[82:85]
	v_mfma_f32_16x16x32_f16 v[90:93], v[224:227], v[176:179], v[90:93]
	v_mfma_f32_16x16x32_f16 v[94:97], v[224:227], v[184:187], v[94:97]
	v_mfma_f32_16x16x32_f16 v[26:29], v[200:203], v[180:183], v[26:29]
	v_mfma_f32_16x16x32_f16 v[38:41], v[200:203], v[188:191], v[38:41]
	v_mfma_f32_16x16x32_f16 v[50:53], v[212:215], v[180:183], v[50:53]
	v_mfma_f32_16x16x32_f16 v[62:65], v[212:215], v[188:191], v[62:65]
	v_mfma_f32_16x16x32_f16 v[74:77], v[220:223], v[180:183], v[74:77]
	v_mfma_f32_16x16x32_f16 v[82:85], v[220:223], v[188:191], v[82:85]
	v_mfma_f32_16x16x32_f16 v[90:93], v[228:231], v[180:183], v[90:93]
	v_mfma_f32_16x16x32_f16 v[94:97], v[228:231], v[188:191], v[94:97]
	s_barrier
	v_lshl_add_u64 v[176:177], v[250:251], 0, s[42:43]
	s_mov_b32 m0, s86
	global_load_lds_dwordx4 v[176:177], off
	s_mov_b32 m0, s87
	v_lshl_add_u64 v[176:177], v[252:253], 0, s[42:43]
	global_load_lds_dwordx4 v[176:177], off
	s_waitcnt vmcnt(6)
	s_barrier
	v_mfma_f32_16x16x32_f16 v[98:101], v[196:199], v[232:235], v[98:101]
	v_mfma_f32_16x16x32_f16 v[102:105], v[196:199], v[240:243], v[102:105]
	v_mfma_f32_16x16x32_f16 v[106:109], v[204:207], v[232:235], v[106:109]
	v_mfma_f32_16x16x32_f16 v[110:113], v[204:207], v[240:243], v[110:113]
	v_mfma_f32_16x16x32_f16 v[114:117], v[216:219], v[232:235], v[114:117]
	v_mfma_f32_16x16x32_f16 v[118:121], v[216:219], v[240:243], v[118:121]
	v_mfma_f32_16x16x32_f16 v[122:125], v[224:227], v[232:235], v[122:125]
	v_mfma_f32_16x16x32_f16 v[126:129], v[224:227], v[240:243], v[126:129]
	v_mfma_f32_16x16x32_f16 v[98:101], v[200:203], v[236:239], v[98:101]
	v_mfma_f32_16x16x32_f16 v[102:105], v[200:203], v[244:247], v[102:105]
	v_mfma_f32_16x16x32_f16 v[106:109], v[212:215], v[236:239], v[106:109]
	v_mfma_f32_16x16x32_f16 v[110:113], v[212:215], v[244:247], v[110:113]
	v_mfma_f32_16x16x32_f16 v[114:117], v[220:223], v[236:239], v[114:117]
	v_mfma_f32_16x16x32_f16 v[118:121], v[220:223], v[244:247], v[118:121]
	v_mfma_f32_16x16x32_f16 v[122:125], v[228:231], v[236:239], v[122:125]
	v_mfma_f32_16x16x32_f16 v[126:129], v[228:231], v[244:247], v[126:129]
	s_add_i32 s48, s48, 2
	s_add_u32 s46, s46, 0x100
	s_addc_u32 s47, s47, 0
	s_cmp_lt_u32 s48, 4
	s_barrier
	s_cbranch_scc1 .LBB7_239
	s_add_u32 s0, s0, 0x20380
	s_addc_u32 s1, s1, 0
	v_readfirstlane_b32 s5, v174
	v_lshl_add_u64 v[130:131], v[130:131], 1, s[0:1]
	s_mov_b32 m0, s5
	ds_read_b128 v[134:137], v169
	ds_read_b128 v[138:141], v170
	ds_read_b128 v[152:155], v171
	ds_read_b128 v[156:159], v172
	ds_read_b128 v[166:169], v173
	ds_read_b128 v[176:179], v173 offset:1024
	ds_read_b128 v[180:183], v173 offset:2048
	ds_read_b128 v[184:187], v173 offset:3072
	ds_read_b128 v[188:191], v173 offset:4096
	ds_read_b128 v[196:199], v173 offset:5120
	ds_read_b128 v[200:203], v173 offset:6144
	ds_read_b128 v[204:207], v173 offset:7168
	global_load_lds_dwordx4 v[130:131], off
	v_lshl_add_u64 v[130:131], v[132:133], 1, s[0:1]
	v_readfirstlane_b32 s0, v175
	s_mov_b32 m0, s0
	s_nop 0
	global_load_lds_dwordx4 v[130:131], off
	s_barrier
	s_waitcnt lgkmcnt(0)
	v_mfma_f32_16x16x32_f16 v[2:5], v[166:169], v[134:137], v[2:5]
	v_mfma_f32_16x16x32_f16 v[42:45], v[188:191], v[152:155], v[42:45]
	v_mfma_f32_16x16x32_f16 v[54:57], v[200:203], v[134:137], v[54:57]
	v_mfma_f32_16x16x32_f16 v[66:69], v[200:203], v[152:155], v[66:69]
	v_mfma_f32_16x16x32_f16 v[2:5], v[176:179], v[138:141], v[2:5]
	v_mfma_f32_16x16x32_f16 v[6:9], v[166:169], v[152:155], v[6:9]
	v_mfma_f32_16x16x32_f16 v[10:13], v[180:183], v[134:137], v[10:13]
	v_mfma_f32_16x16x32_f16 v[18:21], v[180:183], v[152:155], v[18:21]
	v_mfma_f32_16x16x32_f16 v[30:33], v[188:191], v[134:137], v[30:33]
	v_mfma_f32_16x16x32_f16 v[42:45], v[196:199], v[156:159], v[42:45]
	v_mfma_f32_16x16x32_f16 v[54:57], v[204:207], v[138:141], v[54:57]
	v_mfma_f32_16x16x32_f16 v[66:69], v[204:207], v[156:159], v[66:69]
	v_mfma_f32_16x16x32_f16 v[6:9], v[176:179], v[156:159], v[6:9]
	v_mfma_f32_16x16x32_f16 v[10:13], v[184:187], v[138:141], v[10:13]
	v_mfma_f32_16x16x32_f16 v[18:21], v[184:187], v[156:159], v[18:21]
	v_mfma_f32_16x16x32_f16 v[30:33], v[196:199], v[138:141], v[30:33]
	s_barrier
	ds_read_b128 v[130:133], v161
	ds_read_b128 v[212:215], v162
	ds_read_b128 v[160:163], v163
	ds_read_b128 v[216:219], v164
	s_barrier
	s_waitcnt lgkmcnt(0)
	v_mfma_f32_16x16x32_f16 v[14:17], v[166:169], v[130:133], v[14:17]
	v_mfma_f32_16x16x32_f16 v[78:81], v[200:203], v[130:133], v[78:81]
	v_mfma_f32_16x16x32_f16 v[14:17], v[176:179], v[212:215], v[14:17]
	v_mfma_f32_16x16x32_f16 v[22:25], v[166:169], v[160:163], v[22:25]
	v_mfma_f32_16x16x32_f16 v[34:37], v[180:183], v[130:133], v[34:37]
	v_mfma_f32_16x16x32_f16 v[46:49], v[180:183], v[160:163], v[46:49]
	v_mfma_f32_16x16x32_f16 v[58:61], v[188:191], v[130:133], v[58:61]
	v_mfma_f32_16x16x32_f16 v[70:73], v[188:191], v[160:163], v[70:73]
	v_mfma_f32_16x16x32_f16 v[164:167], v[204:207], v[212:215], v[78:81]
	v_mfma_f32_16x16x32_f16 v[78:81], v[200:203], v[160:163], v[86:89]
	v_mfma_f32_16x16x32_f16 v[22:25], v[176:179], v[216:219], v[22:25]
	v_mfma_f32_16x16x32_f16 v[34:37], v[184:187], v[212:215], v[34:37]
	v_mfma_f32_16x16x32_f16 v[46:49], v[184:187], v[216:219], v[46:49]
	v_mfma_f32_16x16x32_f16 v[58:61], v[196:199], v[212:215], v[58:61]
	v_mfma_f32_16x16x32_f16 v[70:73], v[196:199], v[216:219], v[70:73]
	v_mfma_f32_16x16x32_f16 v[86:89], v[204:207], v[216:219], v[78:81]
	s_barrier
	s_nop 0
	ds_read_b128 v[78:81], v173 offset:16384
	ds_read_b128 v[168:171], v173 offset:17408
	ds_read_b128 v[174:177], v173 offset:18432
	ds_read_b128 v[178:181], v173 offset:19456
	ds_read_b128 v[182:185], v173 offset:20480
	ds_read_b128 v[186:189], v173 offset:21504
	ds_read_b128 v[190:193], v173 offset:22528
	ds_read_b128 v[196:199], v173 offset:23552
	s_waitcnt vmcnt(4)
	s_barrier
	s_waitcnt lgkmcnt(0)
	v_mfma_f32_16x16x32_f16 v[26:29], v[78:81], v[134:137], v[26:29]
	v_mfma_f32_16x16x32_f16 v[38:41], v[78:81], v[152:155], v[38:41]
	v_mfma_f32_16x16x32_f16 v[26:29], v[168:171], v[138:141], v[26:29]
	v_mfma_f32_16x16x32_f16 v[38:41], v[168:171], v[156:159], v[38:41]
	v_mfma_f32_16x16x32_f16 v[50:53], v[174:177], v[134:137], v[50:53]
	v_mfma_f32_16x16x32_f16 v[62:65], v[174:177], v[152:155], v[62:65]
	v_mfma_f32_16x16x32_f16 v[74:77], v[182:185], v[134:137], v[74:77]
	v_mfma_f32_16x16x32_f16 v[82:85], v[182:185], v[152:155], v[82:85]
	v_mfma_f32_16x16x32_f16 v[90:93], v[190:193], v[134:137], v[90:93]
	v_mfma_f32_16x16x32_f16 v[94:97], v[190:193], v[152:155], v[94:97]
	v_mfma_f32_16x16x32_f16 v[50:53], v[178:181], v[138:141], v[50:53]
	v_mfma_f32_16x16x32_f16 v[62:65], v[178:181], v[156:159], v[62:65]
	v_mfma_f32_16x16x32_f16 v[74:77], v[186:189], v[138:141], v[74:77]
	v_mfma_f32_16x16x32_f16 v[82:85], v[186:189], v[156:159], v[82:85]
	v_mfma_f32_16x16x32_f16 v[90:93], v[196:199], v[138:141], v[90:93]
	v_mfma_f32_16x16x32_f16 v[94:97], v[196:199], v[156:159], v[94:97]
	v_mfma_f32_16x16x32_f16 v[98:101], v[78:81], v[130:133], v[98:101]
	v_mfma_f32_16x16x32_f16 v[78:81], v[78:81], v[160:163], v[102:105]
	v_mfma_f32_16x16x32_f16 v[102:105], v[168:171], v[216:219], v[78:81]
	v_mfma_f32_16x16x32_f16 v[78:81], v[174:177], v[130:133], v[106:109]
	v_mfma_f32_16x16x32_f16 v[106:109], v[178:181], v[212:215], v[78:81]
	v_mfma_f32_16x16x32_f16 v[78:81], v[174:177], v[160:163], v[110:113]
	v_mfma_f32_16x16x32_f16 v[200:203], v[178:181], v[216:219], v[78:81]
	v_mfma_f32_16x16x32_f16 v[78:81], v[182:185], v[130:133], v[114:117]
	v_mfma_f32_16x16x32_f16 v[204:207], v[186:189], v[212:215], v[78:81]
	v_mfma_f32_16x16x32_f16 v[78:81], v[182:185], v[160:163], v[118:121]
	v_mfma_f32_16x16x32_f16 v[220:223], v[186:189], v[216:219], v[78:81]
	v_mfma_f32_16x16x32_f16 v[78:81], v[190:193], v[130:133], v[122:125]
	v_mfma_f32_16x16x32_f16 v[98:101], v[168:171], v[212:215], v[98:101]
	v_mfma_f32_16x16x32_f16 v[212:215], v[196:199], v[212:215], v[78:81]
	v_mfma_f32_16x16x32_f16 v[78:81], v[190:193], v[160:163], v[126:129]
	v_mfma_f32_16x16x32_f16 v[196:199], v[196:199], v[216:219], v[78:81]
	s_barrier
	ds_read_b128 v[110:113], v148
	ds_read_b128 v[130:133], v149
	ds_read_b128 v[216:219], v150
	ds_read_b128 v[224:227], v151
	s_nop 0
	ds_read_b128 v[78:81], v173 offset:32768
	ds_read_b128 v[114:117], v173 offset:33792
	ds_read_b128 v[118:121], v173 offset:34816
	ds_read_b128 v[134:137], v173 offset:35840
	ds_read_b128 v[138:141], v173 offset:36864
	ds_read_b128 v[168:171], v173 offset:37888
	ds_read_b128 v[174:177], v173 offset:38912
	ds_read_b128 v[228:231], v173 offset:39936
	s_waitcnt vmcnt(2)
	s_barrier
	s_waitcnt lgkmcnt(0)
	v_mfma_f32_16x16x32_f16 v[2:5], v[78:81], v[110:113], v[2:5]
	v_mfma_f32_16x16x32_f16 v[190:193], v[114:117], v[130:133], v[2:5]
	v_mfma_f32_16x16x32_f16 v[2:5], v[78:81], v[216:219], v[6:9]
	v_mfma_f32_16x16x32_f16 v[158:161], v[114:117], v[224:227], v[2:5]
	v_mfma_f32_16x16x32_f16 v[2:5], v[118:121], v[110:113], v[10:13]
	v_mfma_f32_16x16x32_f16 v[186:189], v[134:137], v[130:133], v[2:5]
	v_mfma_f32_16x16x32_f16 v[2:5], v[118:121], v[216:219], v[18:21]
	v_mfma_f32_16x16x32_f16 v[154:157], v[134:137], v[224:227], v[2:5]
	v_mfma_f32_16x16x32_f16 v[2:5], v[138:141], v[110:113], v[30:33]
	v_mfma_f32_16x16x32_f16 v[182:185], v[168:171], v[130:133], v[2:5]
	v_mfma_f32_16x16x32_f16 v[2:5], v[138:141], v[216:219], v[42:45]
	v_mfma_f32_16x16x32_f16 v[150:153], v[168:171], v[224:227], v[2:5]
	v_mfma_f32_16x16x32_f16 v[2:5], v[174:177], v[110:113], v[54:57]
	v_mfma_f32_16x16x32_f16 v[178:181], v[228:231], v[130:133], v[2:5]
	v_mfma_f32_16x16x32_f16 v[2:5], v[174:177], v[216:219], v[66:69]
	v_mfma_f32_16x16x32_f16 v[146:149], v[228:231], v[224:227], v[2:5]
	s_barrier
	s_nop 4
	ds_read_b128 v[2:5], v142
	ds_read_b128 v[6:9], v143
	ds_read_b128 v[10:13], v144
	ds_read_b128 v[18:21], v145
	s_waitcnt vmcnt(0)
	s_barrier
	s_waitcnt lgkmcnt(0)
	v_mfma_f32_16x16x32_f16 v[14:17], v[78:81], v[2:5], v[14:17]
	v_mfma_f32_16x16x32_f16 v[126:129], v[114:117], v[6:9], v[14:17]
	v_mfma_f32_16x16x32_f16 v[14:17], v[78:81], v[10:13], v[22:25]
	v_mfma_f32_16x16x32_f16 v[78:81], v[114:117], v[18:21], v[14:17]
	v_mfma_f32_16x16x32_f16 v[14:17], v[118:121], v[2:5], v[34:37]
	v_mfma_f32_16x16x32_f16 v[122:125], v[134:137], v[6:9], v[14:17]
	v_mfma_f32_16x16x32_f16 v[14:17], v[118:121], v[10:13], v[46:49]
	v_mfma_f32_16x16x32_f16 v[66:69], v[134:137], v[18:21], v[14:17]
	v_mfma_f32_16x16x32_f16 v[14:17], v[138:141], v[2:5], v[58:61]
	v_mfma_f32_16x16x32_f16 v[118:121], v[168:171], v[6:9], v[14:17]
	v_mfma_f32_16x16x32_f16 v[14:17], v[138:141], v[10:13], v[70:73]
	v_mfma_f32_16x16x32_f16 v[54:57], v[168:171], v[18:21], v[14:17]
	v_mfma_f32_16x16x32_f16 v[14:17], v[174:177], v[2:5], v[164:167]
	v_mfma_f32_16x16x32_f16 v[114:117], v[228:231], v[6:9], v[14:17]
	v_mfma_f32_16x16x32_f16 v[14:17], v[174:177], v[10:13], v[86:89]
	v_mfma_f32_16x16x32_f16 v[42:45], v[228:231], v[18:21], v[14:17]
	s_barrier
	s_nop 4
	ds_read_b128 v[14:17], v173 offset:49152
	ds_read_b128 v[22:25], v173 offset:50176
	ds_read_b128 v[30:33], v173 offset:51200
	ds_read_b128 v[34:37], v173 offset:52224
	ds_read_b128 v[46:49], v173 offset:53248
	ds_read_b128 v[58:61], v173 offset:54272
	ds_read_b128 v[70:73], v173 offset:55296
	ds_read_b128 v[86:89], v173 offset:56320
	s_barrier
	s_waitcnt lgkmcnt(0)
	v_mfma_f32_16x16x32_f16 v[26:29], v[14:17], v[110:113], v[26:29]
	v_mfma_f32_16x16x32_f16 v[174:177], v[22:25], v[130:133], v[26:29]
	v_mfma_f32_16x16x32_f16 v[26:29], v[14:17], v[216:219], v[38:41]
	v_mfma_f32_16x16x32_f16 v[142:145], v[22:25], v[224:227], v[26:29]
	v_mfma_f32_16x16x32_f16 v[26:29], v[30:33], v[110:113], v[50:53]
	v_mfma_f32_16x16x32_f16 v[170:173], v[34:37], v[130:133], v[26:29]
	v_mfma_f32_16x16x32_f16 v[26:29], v[30:33], v[216:219], v[62:65]
	v_mfma_f32_16x16x32_f16 v[138:141], v[34:37], v[224:227], v[26:29]
	v_mfma_f32_16x16x32_f16 v[26:29], v[46:49], v[110:113], v[74:77]
	v_mfma_f32_16x16x32_f16 v[166:169], v[58:61], v[130:133], v[26:29]
	v_mfma_f32_16x16x32_f16 v[26:29], v[46:49], v[216:219], v[82:85]
	v_mfma_f32_16x16x32_f16 v[134:137], v[58:61], v[224:227], v[26:29]
	v_mfma_f32_16x16x32_f16 v[26:29], v[70:73], v[110:113], v[90:93]
	v_mfma_f32_16x16x32_f16 v[162:165], v[86:89], v[130:133], v[26:29]
	v_mfma_f32_16x16x32_f16 v[26:29], v[70:73], v[216:219], v[94:97]
	v_mfma_f32_16x16x32_f16 v[130:133], v[86:89], v[224:227], v[26:29]
	v_mfma_f32_16x16x32_f16 v[26:29], v[14:17], v[2:5], v[98:101]
	v_mfma_f32_16x16x32_f16 v[14:17], v[14:17], v[10:13], v[102:105]
	v_mfma_f32_16x16x32_f16 v[38:41], v[22:25], v[18:21], v[14:17]
	v_mfma_f32_16x16x32_f16 v[14:17], v[30:33], v[2:5], v[106:109]
	v_mfma_f32_16x16x32_f16 v[106:109], v[34:37], v[6:9], v[14:17]
	v_mfma_f32_16x16x32_f16 v[14:17], v[30:33], v[10:13], v[200:203]
	v_mfma_f32_16x16x32_f16 v[110:113], v[22:25], v[6:9], v[26:29]
	v_mfma_f32_16x16x32_f16 v[26:29], v[34:37], v[18:21], v[14:17]
	v_mfma_f32_16x16x32_f16 v[14:17], v[46:49], v[2:5], v[204:207]
	v_mfma_f32_16x16x32_f16 v[2:5], v[70:73], v[2:5], v[212:215]
	v_mfma_f32_16x16x32_f16 v[102:105], v[58:61], v[6:9], v[14:17]
	v_mfma_f32_16x16x32_f16 v[14:17], v[46:49], v[10:13], v[220:223]
	v_mfma_f32_16x16x32_f16 v[98:101], v[86:89], v[6:9], v[2:5]
	v_mfma_f32_16x16x32_f16 v[2:5], v[70:73], v[10:13], v[196:199]
	v_mfma_f32_16x16x32_f16 v[14:17], v[58:61], v[18:21], v[14:17]
	v_mfma_f32_16x16x32_f16 v[2:5], v[86:89], v[18:21], v[2:5]
	s_cmpk_gt_u32 s65, 0xff
	s_barrier
	s_cbranch_scc1 .LBB7_242
	s_barrier

.LBB8_41:
	ds_read_b128 v[182:185], v171
	ds_read_b128 v[186:189], v173
	ds_read_b128 v[190:193], v174
	ds_read_b128 v[194:197], v175
	v_add_u32_e32 v177, 0xc000, v148
	v_lshl_add_u64 v[246:247], v[134:135], 0, s[44:45]
	v_add_u32_e32 v176, s48, v170
	v_lshl_add_u64 v[178:179], v[246:247], 0, s[28:29]
	s_mov_b32 m0, s75
	ds_read_b128 v[198:201], v176
	ds_read_b128 v[202:205], v176 offset:1024
	ds_read_b128 v[206:209], v176 offset:2048
	ds_read_b128 v[210:213], v176 offset:3072
	ds_read_b128 v[214:217], v176 offset:4096
	ds_read_b128 v[218:221], v176 offset:5120
	ds_read_b128 v[222:225], v176 offset:6144
	ds_read_b128 v[226:229], v176 offset:7168
	global_load_lds_dwordx4 v[178:179], off
	v_add_u32_e32 v178, 0xe000, v148
	v_lshl_add_u64 v[248:249], v[136:137], 0, s[44:45]
	s_mov_b32 m0, s76
	v_lshl_add_u64 v[230:231], v[248:249], 0, s[28:29]
	global_load_lds_dwordx4 v[230:231], off
	s_waitcnt lgkmcnt(8)
	s_barrier
	s_waitcnt lgkmcnt(0)
	v_mfma_f32_16x16x32_f16 v[126:129], v[198:201], v[182:185], v[126:129]
	v_mfma_f32_16x16x32_f16 v[122:125], v[198:201], v[190:193], v[122:125]
	v_mfma_f32_16x16x32_f16 v[118:121], v[206:209], v[182:185], v[118:121]
	v_mfma_f32_16x16x32_f16 v[114:117], v[206:209], v[190:193], v[114:117]
	v_mfma_f32_16x16x32_f16 v[110:113], v[214:217], v[182:185], v[110:113]
	v_mfma_f32_16x16x32_f16 v[106:109], v[214:217], v[190:193], v[106:109]
	v_mfma_f32_16x16x32_f16 v[102:105], v[222:225], v[182:185], v[102:105]
	v_mfma_f32_16x16x32_f16 v[98:101], v[222:225], v[190:193], v[98:101]
	v_mfma_f32_16x16x32_f16 v[126:129], v[202:205], v[186:189], v[126:129]
	v_mfma_f32_16x16x32_f16 v[122:125], v[202:205], v[194:197], v[122:125]
	v_mfma_f32_16x16x32_f16 v[118:121], v[210:213], v[186:189], v[118:121]
	v_mfma_f32_16x16x32_f16 v[114:117], v[210:213], v[194:197], v[114:117]
	v_mfma_f32_16x16x32_f16 v[110:113], v[218:221], v[186:189], v[110:113]
	v_mfma_f32_16x16x32_f16 v[106:109], v[218:221], v[194:197], v[106:109]
	v_mfma_f32_16x16x32_f16 v[102:105], v[226:229], v[186:189], v[102:105]
	v_mfma_f32_16x16x32_f16 v[98:101], v[226:229], v[194:197], v[98:101]
	s_barrier
	v_lshl_add_u64 v[250:251], v[138:139], 0, s[44:45]
	v_lshl_add_u64 v[252:253], v[250:251], 0, s[30:31]
	s_mov_b32 m0, s77
	ds_read_b128 v[230:233], v162
	ds_read_b128 v[234:237], v163
	ds_read_b128 v[238:241], v164
	ds_read_b128 v[242:245], v165
	global_load_lds_dwordx4 v[252:253], off
	v_lshl_add_u64 v[252:253], v[140:141], 0, s[44:45]
	s_mov_b32 m0, s78
	v_lshl_add_u64 v[254:255], v[252:253], 0, s[30:31]
	global_load_lds_dwordx4 v[254:255], off
	s_barrier
	s_waitcnt lgkmcnt(0)
	v_mfma_f32_16x16x32_f16 v[94:97], v[198:201], v[230:233], v[94:97]
	v_mfma_f32_16x16x32_f16 v[90:93], v[198:201], v[238:241], v[90:93]
	v_mfma_f32_16x16x32_f16 v[86:89], v[206:209], v[230:233], v[86:89]
	v_mfma_f32_16x16x32_f16 v[82:85], v[206:209], v[238:241], v[82:85]
	v_mfma_f32_16x16x32_f16 v[78:81], v[214:217], v[230:233], v[78:81]
	v_mfma_f32_16x16x32_f16 v[74:77], v[214:217], v[238:241], v[74:77]
	v_mfma_f32_16x16x32_f16 v[70:73], v[222:225], v[230:233], v[70:73]
	v_mfma_f32_16x16x32_f16 v[66:69], v[222:225], v[238:241], v[66:69]
	v_mfma_f32_16x16x32_f16 v[94:97], v[202:205], v[234:237], v[94:97]
	v_mfma_f32_16x16x32_f16 v[90:93], v[202:205], v[242:245], v[90:93]
	v_mfma_f32_16x16x32_f16 v[86:89], v[210:213], v[234:237], v[86:89]
	v_mfma_f32_16x16x32_f16 v[82:85], v[210:213], v[242:245], v[82:85]
	v_mfma_f32_16x16x32_f16 v[78:81], v[218:221], v[234:237], v[78:81]
	v_mfma_f32_16x16x32_f16 v[74:77], v[218:221], v[242:245], v[74:77]
	v_mfma_f32_16x16x32_f16 v[70:73], v[226:229], v[234:237], v[70:73]
	v_mfma_f32_16x16x32_f16 v[66:69], v[226:229], v[242:245], v[66:69]
	v_lshl_add_u64 v[254:255], v[246:247], 0, s[30:31]
	s_mov_b32 m0, s79
	s_barrier
	ds_read_b128 v[198:201], v176 offset:16384
	ds_read_b128 v[202:205], v176 offset:17408
	ds_read_b128 v[206:209], v176 offset:18432
	ds_read_b128 v[210:213], v176 offset:19456
	ds_read_b128 v[214:217], v176 offset:20480
	ds_read_b128 v[218:221], v176 offset:21504
	ds_read_b128 v[222:225], v176 offset:22528
	ds_read_b128 v[226:229], v176 offset:23552
	global_load_lds_dwordx4 v[254:255], off
	s_mov_b32 m0, s80
	v_lshl_add_u64 v[254:255], v[248:249], 0, s[30:31]
	global_load_lds_dwordx4 v[254:255], off
	s_barrier
	s_waitcnt lgkmcnt(0)
	v_mfma_f32_16x16x32_f16 v[62:65], v[198:201], v[182:185], v[62:65]
	v_mfma_f32_16x16x32_f16 v[58:61], v[198:201], v[190:193], v[58:61]
	v_mfma_f32_16x16x32_f16 v[54:57], v[206:209], v[182:185], v[54:57]
	v_mfma_f32_16x16x32_f16 v[50:53], v[206:209], v[190:193], v[50:53]
	v_mfma_f32_16x16x32_f16 v[46:49], v[214:217], v[182:185], v[46:49]
	v_mfma_f32_16x16x32_f16 v[42:45], v[214:217], v[190:193], v[42:45]
	v_mfma_f32_16x16x32_f16 v[38:41], v[222:225], v[182:185], v[38:41]
	v_mfma_f32_16x16x32_f16 v[34:37], v[222:225], v[190:193], v[34:37]
	v_mfma_f32_16x16x32_f16 v[62:65], v[202:205], v[186:189], v[62:65]
	v_mfma_f32_16x16x32_f16 v[58:61], v[202:205], v[194:197], v[58:61]
	v_mfma_f32_16x16x32_f16 v[54:57], v[210:213], v[186:189], v[54:57]
	v_mfma_f32_16x16x32_f16 v[50:53], v[210:213], v[194:197], v[50:53]
	v_mfma_f32_16x16x32_f16 v[46:49], v[218:221], v[186:189], v[46:49]
	v_mfma_f32_16x16x32_f16 v[42:45], v[218:221], v[194:197], v[42:45]
	v_mfma_f32_16x16x32_f16 v[38:41], v[226:229], v[186:189], v[38:41]
	v_mfma_f32_16x16x32_f16 v[34:37], v[226:229], v[194:197], v[34:37]
	s_barrier
	v_lshl_add_u64 v[182:183], v[250:251], 0, s[34:35]
	s_mov_b32 m0, s81
	global_load_lds_dwordx4 v[182:183], off
	s_mov_b32 m0, s82
	v_lshl_add_u64 v[182:183], v[252:253], 0, s[34:35]
	global_load_lds_dwordx4 v[182:183], off
	s_waitcnt vmcnt(6)
	s_barrier
	v_mfma_f32_16x16x32_f16 v[30:33], v[198:201], v[230:233], v[30:33]
	v_mfma_f32_16x16x32_f16 v[26:29], v[198:201], v[238:241], v[26:29]
	v_mfma_f32_16x16x32_f16 v[22:25], v[206:209], v[230:233], v[22:25]
	v_mfma_f32_16x16x32_f16 v[18:21], v[206:209], v[238:241], v[18:21]
	v_mfma_f32_16x16x32_f16 v[14:17], v[214:217], v[230:233], v[14:17]
	v_mfma_f32_16x16x32_f16 v[10:13], v[214:217], v[238:241], v[10:13]
	v_mfma_f32_16x16x32_f16 v[6:9], v[222:225], v[230:233], v[6:9]
	v_mfma_f32_16x16x32_f16 v[2:5], v[222:225], v[238:241], v[2:5]
	v_mfma_f32_16x16x32_f16 v[30:33], v[202:205], v[234:237], v[30:33]
	v_mfma_f32_16x16x32_f16 v[26:29], v[202:205], v[242:245], v[26:29]
	v_mfma_f32_16x16x32_f16 v[22:25], v[210:213], v[234:237], v[22:25]
	v_mfma_f32_16x16x32_f16 v[18:21], v[210:213], v[242:245], v[18:21]
	v_mfma_f32_16x16x32_f16 v[14:17], v[218:221], v[234:237], v[14:17]
	v_mfma_f32_16x16x32_f16 v[10:13], v[218:221], v[242:245], v[10:13]
	v_mfma_f32_16x16x32_f16 v[6:9], v[226:229], v[234:237], v[6:9]
	v_mfma_f32_16x16x32_f16 v[2:5], v[226:229], v[242:245], v[2:5]
	s_barrier
	ds_read_b128 v[182:185], v144
	ds_read_b128 v[186:189], v145
	ds_read_b128 v[190:193], v146
	ds_read_b128 v[194:197], v147
	v_lshl_add_u64 v[230:231], v[246:247], 0, s[34:35]
	s_mov_b32 m0, s83
	ds_read_b128 v[198:201], v176 offset:32768
	ds_read_b128 v[202:205], v176 offset:33792
	ds_read_b128 v[206:209], v176 offset:34816
	ds_read_b128 v[210:213], v176 offset:35840
	ds_read_b128 v[214:217], v176 offset:36864
	ds_read_b128 v[218:221], v176 offset:37888
	ds_read_b128 v[222:225], v176 offset:38912
	ds_read_b128 v[226:229], v176 offset:39936
	global_load_lds_dwordx4 v[230:231], off
	s_mov_b32 m0, s84
	v_lshl_add_u64 v[230:231], v[248:249], 0, s[34:35]
	global_load_lds_dwordx4 v[230:231], off
	s_waitcnt lgkmcnt(8)
	s_barrier
	s_waitcnt lgkmcnt(0)
	v_mfma_f32_16x16x32_f16 v[126:129], v[198:201], v[182:185], v[126:129]
	v_mfma_f32_16x16x32_f16 v[122:125], v[198:201], v[190:193], v[122:125]
	v_mfma_f32_16x16x32_f16 v[118:121], v[206:209], v[182:185], v[118:121]
	v_mfma_f32_16x16x32_f16 v[114:117], v[206:209], v[190:193], v[114:117]
	v_mfma_f32_16x16x32_f16 v[110:113], v[214:217], v[182:185], v[110:113]
	v_mfma_f32_16x16x32_f16 v[106:109], v[214:217], v[190:193], v[106:109]
	v_mfma_f32_16x16x32_f16 v[102:105], v[222:225], v[182:185], v[102:105]
	v_mfma_f32_16x16x32_f16 v[98:101], v[222:225], v[190:193], v[98:101]
	v_mfma_f32_16x16x32_f16 v[126:129], v[202:205], v[186:189], v[126:129]
	v_mfma_f32_16x16x32_f16 v[122:125], v[202:205], v[194:197], v[122:125]
	v_mfma_f32_16x16x32_f16 v[118:121], v[210:213], v[186:189], v[118:121]
	v_mfma_f32_16x16x32_f16 v[114:117], v[210:213], v[194:197], v[114:117]
	v_mfma_f32_16x16x32_f16 v[110:113], v[218:221], v[186:189], v[110:113]
	v_mfma_f32_16x16x32_f16 v[106:109], v[218:221], v[194:197], v[106:109]
	v_mfma_f32_16x16x32_f16 v[102:105], v[226:229], v[186:189], v[102:105]
	v_mfma_f32_16x16x32_f16 v[98:101], v[226:229], v[194:197], v[98:101]
	s_barrier
	v_lshl_add_u64 v[254:255], v[250:251], 0, s[36:37]
	s_mov_b32 m0, s85
	ds_read_b128 v[230:233], v150
	ds_read_b128 v[234:237], v151
	ds_read_b128 v[238:241], v152
	ds_read_b128 v[242:245], v153
	global_load_lds_dwordx4 v[254:255], off
	s_mov_b32 m0, s86
	v_lshl_add_u64 v[254:255], v[252:253], 0, s[36:37]
	global_load_lds_dwordx4 v[254:255], off
	s_barrier
	s_waitcnt lgkmcnt(0)
	v_mfma_f32_16x16x32_f16 v[94:97], v[198:201], v[230:233], v[94:97]
	v_mfma_f32_16x16x32_f16 v[90:93], v[198:201], v[238:241], v[90:93]
	v_mfma_f32_16x16x32_f16 v[86:89], v[206:209], v[230:233], v[86:89]
	v_mfma_f32_16x16x32_f16 v[82:85], v[206:209], v[238:241], v[82:85]
	v_mfma_f32_16x16x32_f16 v[78:81], v[214:217], v[230:233], v[78:81]
	v_mfma_f32_16x16x32_f16 v[74:77], v[214:217], v[238:241], v[74:77]
	v_mfma_f32_16x16x32_f16 v[70:73], v[222:225], v[230:233], v[70:73]
	v_mfma_f32_16x16x32_f16 v[66:69], v[222:225], v[238:241], v[66:69]
	v_mfma_f32_16x16x32_f16 v[94:97], v[202:205], v[234:237], v[94:97]
	v_mfma_f32_16x16x32_f16 v[90:93], v[202:205], v[242:245], v[90:93]
	v_mfma_f32_16x16x32_f16 v[86:89], v[210:213], v[234:237], v[86:89]
	v_mfma_f32_16x16x32_f16 v[82:85], v[210:213], v[242:245], v[82:85]
	v_mfma_f32_16x16x32_f16 v[78:81], v[218:221], v[234:237], v[78:81]
	v_mfma_f32_16x16x32_f16 v[74:77], v[218:221], v[242:245], v[74:77]
	v_mfma_f32_16x16x32_f16 v[70:73], v[226:229], v[234:237], v[70:73]
	v_mfma_f32_16x16x32_f16 v[66:69], v[226:229], v[242:245], v[66:69]
	v_lshl_add_u64 v[246:247], v[246:247], 0, s[36:37]
	s_mov_b32 m0, s87
	s_barrier
	ds_read_b128 v[198:201], v176 offset:49152
	ds_read_b128 v[202:205], v176 offset:50176
	ds_read_b128 v[206:209], v176 offset:51200
	ds_read_b128 v[210:213], v176 offset:52224
	ds_read_b128 v[214:217], v176 offset:53248
	ds_read_b128 v[218:221], v176 offset:54272
	ds_read_b128 v[222:225], v176 offset:55296
	ds_read_b128 v[226:229], v176 offset:56320
	global_load_lds_dwordx4 v[246:247], off
	s_mov_b32 m0, s88
	v_lshl_add_u64 v[246:247], v[248:249], 0, s[36:37]
	global_load_lds_dwordx4 v[246:247], off
	s_barrier
	s_waitcnt lgkmcnt(0)
	v_mfma_f32_16x16x32_f16 v[62:65], v[198:201], v[182:185], v[62:65]
	v_mfma_f32_16x16x32_f16 v[58:61], v[198:201], v[190:193], v[58:61]
	v_mfma_f32_16x16x32_f16 v[54:57], v[206:209], v[182:185], v[54:57]
	v_mfma_f32_16x16x32_f16 v[50:53], v[206:209], v[190:193], v[50:53]
	v_mfma_f32_16x16x32_f16 v[46:49], v[214:217], v[182:185], v[46:49]
	v_mfma_f32_16x16x32_f16 v[42:45], v[214:217], v[190:193], v[42:45]
	v_mfma_f32_16x16x32_f16 v[38:41], v[222:225], v[182:185], v[38:41]
	v_mfma_f32_16x16x32_f16 v[34:37], v[222:225], v[190:193], v[34:37]
	v_mfma_f32_16x16x32_f16 v[62:65], v[202:205], v[186:189], v[62:65]
	v_mfma_f32_16x16x32_f16 v[58:61], v[202:205], v[194:197], v[58:61]
	v_mfma_f32_16x16x32_f16 v[54:57], v[210:213], v[186:189], v[54:57]
	v_mfma_f32_16x16x32_f16 v[50:53], v[210:213], v[194:197], v[50:53]
	v_mfma_f32_16x16x32_f16 v[46:49], v[218:221], v[186:189], v[46:49]
	v_mfma_f32_16x16x32_f16 v[42:45], v[218:221], v[194:197], v[42:45]
	v_mfma_f32_16x16x32_f16 v[38:41], v[226:229], v[186:189], v[38:41]
	v_mfma_f32_16x16x32_f16 v[34:37], v[226:229], v[194:197], v[34:37]
	s_barrier
	v_lshl_add_u64 v[182:183], v[250:251], 0, s[38:39]
	s_mov_b32 m0, s89
	global_load_lds_dwordx4 v[182:183], off
	s_mov_b32 m0, s90
	v_lshl_add_u64 v[182:183], v[252:253], 0, s[38:39]
	global_load_lds_dwordx4 v[182:183], off
	s_waitcnt vmcnt(6)
	s_barrier
	v_mfma_f32_16x16x32_f16 v[30:33], v[198:201], v[230:233], v[30:33]
	v_mfma_f32_16x16x32_f16 v[26:29], v[198:201], v[238:241], v[26:29]
	v_mfma_f32_16x16x32_f16 v[22:25], v[206:209], v[230:233], v[22:25]
	v_mfma_f32_16x16x32_f16 v[18:21], v[206:209], v[238:241], v[18:21]
	v_mfma_f32_16x16x32_f16 v[14:17], v[214:217], v[230:233], v[14:17]
	v_mfma_f32_16x16x32_f16 v[10:13], v[214:217], v[238:241], v[10:13]
	v_mfma_f32_16x16x32_f16 v[6:9], v[222:225], v[230:233], v[6:9]
	v_mfma_f32_16x16x32_f16 v[2:5], v[222:225], v[238:241], v[2:5]
	v_mfma_f32_16x16x32_f16 v[30:33], v[202:205], v[234:237], v[30:33]
	v_mfma_f32_16x16x32_f16 v[26:29], v[202:205], v[242:245], v[26:29]
	v_mfma_f32_16x16x32_f16 v[22:25], v[210:213], v[234:237], v[22:25]
	v_mfma_f32_16x16x32_f16 v[18:21], v[210:213], v[242:245], v[18:21]
	v_mfma_f32_16x16x32_f16 v[14:17], v[218:221], v[234:237], v[14:17]
	v_mfma_f32_16x16x32_f16 v[10:13], v[218:221], v[242:245], v[10:13]
	v_mfma_f32_16x16x32_f16 v[6:9], v[226:229], v[234:237], v[6:9]
	v_mfma_f32_16x16x32_f16 v[2:5], v[226:229], v[242:245], v[2:5]
	s_add_i32 s46, s46, 2
	s_add_u32 s44, s44, 0x100
	s_addc_u32 s45, s45, 0
	s_cmp_lt_u32 s46, 4
	s_barrier
	s_cbranch_scc1 .LBB8_41
	s_add_u32 s42, s42, 0x20380
	s_addc_u32 s43, s43, 0
	v_readfirstlane_b32 s44, v177
	v_lshl_add_u64 v[130:131], v[130:131], 1, s[42:43]
	s_mov_b32 m0, s44
	ds_read_b128 v[134:137], v171
	ds_read_b128 v[138:141], v173
	ds_read_b128 v[154:157], v174
	ds_read_b128 v[168:171], v175
	ds_read_b128 v[182:185], v176
	ds_read_b128 v[186:189], v176 offset:1024
	ds_read_b128 v[190:193], v176 offset:2048
	ds_read_b128 v[194:197], v176 offset:3072
	ds_read_b128 v[198:201], v176 offset:4096
	ds_read_b128 v[202:205], v176 offset:5120
	ds_read_b128 v[206:209], v176 offset:6144
	ds_read_b128 v[210:213], v176 offset:7168
	global_load_lds_dwordx4 v[130:131], off
	v_lshl_add_u64 v[130:131], v[132:133], 1, s[42:43]
	v_readfirstlane_b32 s42, v178
	s_mov_b32 m0, s42
	s_nop 0
	global_load_lds_dwordx4 v[130:131], off
	s_barrier
	s_waitcnt lgkmcnt(0)
	v_mfma_f32_16x16x32_f16 v[122:125], v[182:185], v[154:157], v[122:125]
	v_mfma_f32_16x16x32_f16 v[110:113], v[198:201], v[134:137], v[110:113]
	v_mfma_f32_16x16x32_f16 v[98:101], v[206:209], v[154:157], v[98:101]
	v_mfma_f32_16x16x32_f16 v[126:129], v[182:185], v[134:137], v[126:129]
	v_mfma_f32_16x16x32_f16 v[122:125], v[186:189], v[168:171], v[122:125]
	v_mfma_f32_16x16x32_f16 v[118:121], v[190:193], v[134:137], v[118:121]
	v_mfma_f32_16x16x32_f16 v[114:117], v[190:193], v[154:157], v[114:117]
	v_mfma_f32_16x16x32_f16 v[130:133], v[202:205], v[138:141], v[110:113]
	v_mfma_f32_16x16x32_f16 v[106:109], v[198:201], v[154:157], v[106:109]
	v_mfma_f32_16x16x32_f16 v[102:105], v[206:209], v[134:137], v[102:105]
	v_mfma_f32_16x16x32_f16 v[98:101], v[210:213], v[168:171], v[98:101]
	v_mfma_f32_16x16x32_f16 v[126:129], v[186:189], v[138:141], v[126:129]
	v_mfma_f32_16x16x32_f16 v[118:121], v[194:197], v[138:141], v[118:121]
	v_mfma_f32_16x16x32_f16 v[114:117], v[194:197], v[168:171], v[114:117]
	v_mfma_f32_16x16x32_f16 v[214:217], v[202:205], v[168:171], v[106:109]
	v_mfma_f32_16x16x32_f16 v[102:105], v[210:213], v[138:141], v[102:105]
	s_barrier
	ds_read_b128 v[106:109], v162
	ds_read_b128 v[110:113], v163
	ds_read_b128 v[160:163], v164
	ds_read_b128 v[218:221], v165
	s_barrier
	s_waitcnt lgkmcnt(0)
	v_mfma_f32_16x16x32_f16 v[82:85], v[190:193], v[160:163], v[82:85]
	v_mfma_f32_16x16x32_f16 v[78:81], v[198:201], v[106:109], v[78:81]
	v_mfma_f32_16x16x32_f16 v[74:77], v[198:201], v[160:163], v[74:77]
	v_mfma_f32_16x16x32_f16 v[70:73], v[206:209], v[106:109], v[70:73]
	v_mfma_f32_16x16x32_f16 v[66:69], v[206:209], v[160:163], v[66:69]
	v_mfma_f32_16x16x32_f16 v[94:97], v[182:185], v[106:109], v[94:97]
	v_mfma_f32_16x16x32_f16 v[90:93], v[182:185], v[160:163], v[90:93]
	v_mfma_f32_16x16x32_f16 v[86:89], v[190:193], v[106:109], v[86:89]
	v_mfma_f32_16x16x32_f16 v[82:85], v[194:197], v[218:221], v[82:85]
	v_mfma_f32_16x16x32_f16 v[78:81], v[202:205], v[110:113], v[78:81]
	v_mfma_f32_16x16x32_f16 v[74:77], v[202:205], v[218:221], v[74:77]
	v_mfma_f32_16x16x32_f16 v[70:73], v[210:213], v[110:113], v[70:73]
	v_mfma_f32_16x16x32_f16 v[66:69], v[210:213], v[218:221], v[66:69]
	v_mfma_f32_16x16x32_f16 v[222:225], v[186:189], v[110:113], v[94:97]
	v_mfma_f32_16x16x32_f16 v[182:185], v[186:189], v[218:221], v[90:93]
	v_mfma_f32_16x16x32_f16 v[86:89], v[194:197], v[110:113], v[86:89]
	s_barrier
	ds_read_b128 v[90:93], v176 offset:16384
	ds_read_b128 v[94:97], v176 offset:17408
	ds_read_b128 v[186:189], v176 offset:18432
	ds_read_b128 v[190:193], v176 offset:19456
	ds_read_b128 v[194:197], v176 offset:20480
	ds_read_b128 v[198:201], v176 offset:21504
	ds_read_b128 v[202:205], v176 offset:22528
	ds_read_b128 v[206:209], v176 offset:23552
	s_waitcnt vmcnt(4)
	s_barrier
	s_waitcnt lgkmcnt(0)
	v_mfma_f32_16x16x32_f16 v[46:49], v[194:197], v[134:137], v[46:49]
	v_mfma_f32_16x16x32_f16 v[42:45], v[194:197], v[154:157], v[42:45]
	v_mfma_f32_16x16x32_f16 v[38:41], v[202:205], v[134:137], v[38:41]
	v_mfma_f32_16x16x32_f16 v[34:37], v[202:205], v[154:157], v[34:37]
	v_mfma_f32_16x16x32_f16 v[62:65], v[90:93], v[134:137], v[62:65]
	v_mfma_f32_16x16x32_f16 v[58:61], v[90:93], v[154:157], v[58:61]
	v_mfma_f32_16x16x32_f16 v[54:57], v[186:189], v[134:137], v[54:57]
	v_mfma_f32_16x16x32_f16 v[50:53], v[186:189], v[154:157], v[50:53]
	v_mfma_f32_16x16x32_f16 v[46:49], v[198:201], v[138:141], v[46:49]
	v_mfma_f32_16x16x32_f16 v[42:45], v[198:201], v[168:171], v[42:45]
	v_mfma_f32_16x16x32_f16 v[38:41], v[206:209], v[138:141], v[38:41]
	v_mfma_f32_16x16x32_f16 v[34:37], v[206:209], v[168:171], v[34:37]
	v_mfma_f32_16x16x32_f16 v[210:213], v[94:97], v[138:141], v[62:65]
	v_mfma_f32_16x16x32_f16 v[226:229], v[94:97], v[168:171], v[58:61]
	v_mfma_f32_16x16x32_f16 v[230:233], v[190:193], v[138:141], v[54:57]
	v_mfma_f32_16x16x32_f16 v[234:237], v[190:193], v[168:171], v[50:53]
	v_mfma_f32_16x16x32_f16 v[2:5], v[202:205], v[160:163], v[2:5]
	v_mfma_f32_16x16x32_f16 v[30:33], v[90:93], v[106:109], v[30:33]
	v_mfma_f32_16x16x32_f16 v[26:29], v[90:93], v[160:163], v[26:29]
	v_mfma_f32_16x16x32_f16 v[22:25], v[186:189], v[106:109], v[22:25]
	v_mfma_f32_16x16x32_f16 v[18:21], v[186:189], v[160:163], v[18:21]
	v_mfma_f32_16x16x32_f16 v[14:17], v[194:197], v[106:109], v[14:17]
	v_mfma_f32_16x16x32_f16 v[10:13], v[194:197], v[160:163], v[10:13]
	v_mfma_f32_16x16x32_f16 v[6:9], v[202:205], v[106:109], v[6:9]
	v_mfma_f32_16x16x32_f16 v[2:5], v[206:209], v[218:221], v[2:5]
	v_mfma_f32_16x16x32_f16 v[138:141], v[94:97], v[110:113], v[30:33]
	v_mfma_f32_16x16x32_f16 v[168:171], v[94:97], v[218:221], v[26:29]
	v_mfma_f32_16x16x32_f16 v[238:241], v[190:193], v[110:113], v[22:25]
	v_mfma_f32_16x16x32_f16 v[186:189], v[190:193], v[218:221], v[18:21]
	v_mfma_f32_16x16x32_f16 v[190:193], v[198:201], v[110:113], v[14:17]
	v_mfma_f32_16x16x32_f16 v[194:197], v[198:201], v[218:221], v[10:13]
	v_mfma_f32_16x16x32_f16 v[198:201], v[206:209], v[110:113], v[6:9]
	s_barrier
	s_nop 0
	ds_read_b128 v[6:9], v144
	ds_read_b128 v[10:13], v145
	ds_read_b128 v[14:17], v146
	ds_read_b128 v[160:163], v147
	ds_read_b128 v[18:21], v176 offset:32768
	ds_read_b128 v[22:25], v176 offset:33792
	ds_read_b128 v[26:29], v176 offset:34816
	ds_read_b128 v[50:53], v176 offset:35840
	ds_read_b128 v[202:205], v176 offset:36864
	ds_read_b128 v[206:209], v176 offset:37888
	ds_read_b128 v[218:221], v176 offset:38912
	ds_read_b128 v[242:245], v176 offset:39936
	s_waitcnt vmcnt(2)
	s_barrier
	s_waitcnt lgkmcnt(0)
	v_mfma_f32_16x16x32_f16 v[30:33], v[18:21], v[6:9], v[126:129]
	v_mfma_f32_16x16x32_f16 v[154:157], v[22:25], v[10:13], v[30:33]
	v_mfma_f32_16x16x32_f16 v[30:33], v[18:21], v[14:17], v[122:125]
	v_mfma_f32_16x16x32_f16 v[110:113], v[22:25], v[160:163], v[30:33]
	v_mfma_f32_16x16x32_f16 v[30:33], v[26:29], v[6:9], v[118:121]
	v_mfma_f32_16x16x32_f16 v[146:149], v[50:53], v[10:13], v[30:33]
	v_mfma_f32_16x16x32_f16 v[30:33], v[26:29], v[14:17], v[114:117]
	v_mfma_f32_16x16x32_f16 v[106:109], v[50:53], v[160:163], v[30:33]
	v_mfma_f32_16x16x32_f16 v[30:33], v[202:205], v[6:9], v[130:133]
	v_mfma_f32_16x16x32_f16 v[142:145], v[206:209], v[10:13], v[30:33]
	v_mfma_f32_16x16x32_f16 v[30:33], v[202:205], v[14:17], v[214:217]
	v_mfma_f32_16x16x32_f16 v[94:97], v[206:209], v[160:163], v[30:33]
	v_mfma_f32_16x16x32_f16 v[30:33], v[218:221], v[6:9], v[102:105]
	v_mfma_f32_16x16x32_f16 v[134:137], v[242:245], v[10:13], v[30:33]
	v_mfma_f32_16x16x32_f16 v[30:33], v[218:221], v[14:17], v[98:101]
	v_mfma_f32_16x16x32_f16 v[90:93], v[242:245], v[160:163], v[30:33]
	s_barrier
	ds_read_b128 v[102:105], v150
	ds_read_b128 v[114:117], v151
	ds_read_b128 v[118:121], v152
	ds_read_b128 v[126:129], v153
	s_waitcnt vmcnt(0)
	s_barrier
	s_waitcnt lgkmcnt(0)
	v_mfma_f32_16x16x32_f16 v[30:33], v[18:21], v[102:105], v[222:225]
	v_mfma_f32_16x16x32_f16 v[18:21], v[18:21], v[118:121], v[182:185]
	v_mfma_f32_16x16x32_f16 v[62:65], v[22:25], v[114:117], v[30:33]
	v_mfma_f32_16x16x32_f16 v[30:33], v[22:25], v[126:129], v[18:21]
	v_mfma_f32_16x16x32_f16 v[18:21], v[26:29], v[102:105], v[86:89]
	v_mfma_f32_16x16x32_f16 v[58:61], v[50:53], v[114:117], v[18:21]
	v_mfma_f32_16x16x32_f16 v[18:21], v[26:29], v[118:121], v[82:85]
	v_mfma_f32_16x16x32_f16 v[26:29], v[50:53], v[126:129], v[18:21]
	v_mfma_f32_16x16x32_f16 v[18:21], v[202:205], v[102:105], v[78:81]
	v_mfma_f32_16x16x32_f16 v[54:57], v[206:209], v[114:117], v[18:21]
	v_mfma_f32_16x16x32_f16 v[18:21], v[202:205], v[118:121], v[74:77]
	v_mfma_f32_16x16x32_f16 v[22:25], v[206:209], v[126:129], v[18:21]
	v_mfma_f32_16x16x32_f16 v[18:21], v[218:221], v[102:105], v[70:73]
	v_mfma_f32_16x16x32_f16 v[50:53], v[242:245], v[114:117], v[18:21]
	v_mfma_f32_16x16x32_f16 v[18:21], v[218:221], v[118:121], v[66:69]
	v_mfma_f32_16x16x32_f16 v[18:21], v[242:245], v[126:129], v[18:21]
	s_barrier
	ds_read_b128 v[86:89], v176 offset:49152
	ds_read_b128 v[150:153], v176 offset:50176
	ds_read_b128 v[182:185], v176 offset:51200
	ds_read_b128 v[202:205], v176 offset:52224
	ds_read_b128 v[206:209], v176 offset:53248
	ds_read_b128 v[214:217], v176 offset:54272
	ds_read_b128 v[218:221], v176 offset:55296
	ds_read_b128 v[174:177], v176 offset:56320
	s_barrier
	s_waitcnt lgkmcnt(0)
	v_mfma_f32_16x16x32_f16 v[66:69], v[86:89], v[6:9], v[210:213]
	v_mfma_f32_16x16x32_f16 v[130:133], v[150:153], v[10:13], v[66:69]
	v_mfma_f32_16x16x32_f16 v[66:69], v[86:89], v[14:17], v[226:229]
	v_mfma_f32_16x16x32_f16 v[78:81], v[150:153], v[160:163], v[66:69]
	v_mfma_f32_16x16x32_f16 v[66:69], v[182:185], v[6:9], v[230:233]
	v_mfma_f32_16x16x32_f16 v[46:49], v[206:209], v[6:9], v[46:49]
	v_mfma_f32_16x16x32_f16 v[6:9], v[218:221], v[6:9], v[38:41]
	v_mfma_f32_16x16x32_f16 v[122:125], v[202:205], v[10:13], v[66:69]
	v_mfma_f32_16x16x32_f16 v[66:69], v[182:185], v[14:17], v[234:237]
	v_mfma_f32_16x16x32_f16 v[42:45], v[206:209], v[14:17], v[42:45]
	v_mfma_f32_16x16x32_f16 v[82:85], v[174:177], v[10:13], v[6:9]
	v_mfma_f32_16x16x32_f16 v[6:9], v[218:221], v[14:17], v[34:37]
	v_mfma_f32_16x16x32_f16 v[74:77], v[202:205], v[160:163], v[66:69]
	v_mfma_f32_16x16x32_f16 v[98:101], v[214:217], v[10:13], v[46:49]
	v_mfma_f32_16x16x32_f16 v[70:73], v[214:217], v[160:163], v[42:45]
	v_mfma_f32_16x16x32_f16 v[66:69], v[174:177], v[160:163], v[6:9]
	v_mfma_f32_16x16x32_f16 v[6:9], v[86:89], v[102:105], v[138:141]
	v_mfma_f32_16x16x32_f16 v[46:49], v[150:153], v[114:117], v[6:9]
	v_mfma_f32_16x16x32_f16 v[6:9], v[86:89], v[118:121], v[168:171]
	v_mfma_f32_16x16x32_f16 v[14:17], v[150:153], v[126:129], v[6:9]
	v_mfma_f32_16x16x32_f16 v[6:9], v[182:185], v[102:105], v[238:241]
	v_mfma_f32_16x16x32_f16 v[42:45], v[202:205], v[114:117], v[6:9]
	v_mfma_f32_16x16x32_f16 v[6:9], v[182:185], v[118:121], v[186:189]
	v_mfma_f32_16x16x32_f16 v[10:13], v[202:205], v[126:129], v[6:9]
	v_mfma_f32_16x16x32_f16 v[6:9], v[206:209], v[102:105], v[190:193]
	v_mfma_f32_16x16x32_f16 v[38:41], v[214:217], v[114:117], v[6:9]
	v_mfma_f32_16x16x32_f16 v[6:9], v[206:209], v[118:121], v[194:197]
	v_mfma_f32_16x16x32_f16 v[34:37], v[218:221], v[102:105], v[198:201]
	v_mfma_f32_16x16x32_f16 v[2:5], v[218:221], v[118:121], v[2:5]
	v_mfma_f32_16x16x32_f16 v[6:9], v[214:217], v[126:129], v[6:9]
	v_mfma_f32_16x16x32_f16 v[34:37], v[174:177], v[114:117], v[34:37]
	v_mfma_f32_16x16x32_f16 v[2:5], v[174:177], v[126:129], v[2:5]
	s_cmpk_gt_u32 s62, 0xff
	s_barrier
	s_cbranch_scc1 .LBB8_44
	s_barrier

.LBB9_38:
	ds_read_b128 v[176:179], v169
	ds_read_b128 v[180:183], v170
	ds_read_b128 v[184:187], v171
	ds_read_b128 v[188:191], v172
	v_add_u32_e32 v174, 0xc000, v152
	v_lshl_add_u64 v[192:193], v[136:137], 0, s[42:43]
	v_add_u32_e32 v175, 0xe000, v152
	v_add_u32_e32 v173, s39, v168
	v_lshl_add_u64 v[230:231], v[192:193], 0, s[10:11]
	s_mov_b32 m0, s65
	v_lshl_add_u64 v[246:247], v[134:135], 0, s[42:43]
	ds_read_b128 v[198:201], v173
	ds_read_b128 v[202:205], v173 offset:1024
	ds_read_b128 v[206:209], v173 offset:2048
	ds_read_b128 v[210:213], v173 offset:3072
	ds_read_b128 v[214:217], v173 offset:4096
	ds_read_b128 v[218:221], v173 offset:5120
	ds_read_b128 v[222:225], v173 offset:6144
	ds_read_b128 v[226:229], v173 offset:7168
	global_load_lds_dwordx4 v[230:231], off
	s_mov_b32 m0, s66
	v_lshl_add_u64 v[230:231], v[246:247], 0, s[10:11]
	global_load_lds_dwordx4 v[230:231], off
	s_waitcnt lgkmcnt(8)
	s_barrier
	s_waitcnt lgkmcnt(0)
	v_mfma_f32_16x16x32_f16 v[2:5], v[198:201], v[176:179], v[2:5]
	v_mfma_f32_16x16x32_f16 v[6:9], v[198:201], v[184:187], v[6:9]
	v_mfma_f32_16x16x32_f16 v[10:13], v[206:209], v[176:179], v[10:13]
	v_mfma_f32_16x16x32_f16 v[18:21], v[206:209], v[184:187], v[18:21]
	v_mfma_f32_16x16x32_f16 v[30:33], v[214:217], v[176:179], v[30:33]
	v_mfma_f32_16x16x32_f16 v[42:45], v[214:217], v[184:187], v[42:45]
	v_mfma_f32_16x16x32_f16 v[54:57], v[222:225], v[176:179], v[54:57]
	v_mfma_f32_16x16x32_f16 v[66:69], v[222:225], v[184:187], v[66:69]
	v_mfma_f32_16x16x32_f16 v[2:5], v[202:205], v[180:183], v[2:5]
	v_mfma_f32_16x16x32_f16 v[6:9], v[202:205], v[188:191], v[6:9]
	v_mfma_f32_16x16x32_f16 v[10:13], v[210:213], v[180:183], v[10:13]
	v_mfma_f32_16x16x32_f16 v[18:21], v[210:213], v[188:191], v[18:21]
	v_mfma_f32_16x16x32_f16 v[30:33], v[218:221], v[180:183], v[30:33]
	v_mfma_f32_16x16x32_f16 v[42:45], v[218:221], v[188:191], v[42:45]
	v_mfma_f32_16x16x32_f16 v[54:57], v[226:229], v[180:183], v[54:57]
	v_mfma_f32_16x16x32_f16 v[66:69], v[226:229], v[188:191], v[66:69]
	s_barrier
	v_lshl_add_u64 v[248:249], v[140:141], 0, s[42:43]
	v_lshl_add_u64 v[250:251], v[248:249], 0, s[26:27]
	s_mov_b32 m0, s67
	ds_read_b128 v[230:233], v161
	ds_read_b128 v[234:237], v162
	ds_read_b128 v[238:241], v163
	ds_read_b128 v[242:245], v164
	global_load_lds_dwordx4 v[250:251], off
	v_lshl_add_u64 v[250:251], v[138:139], 0, s[42:43]
	s_mov_b32 m0, s68
	v_lshl_add_u64 v[252:253], v[250:251], 0, s[26:27]
	global_load_lds_dwordx4 v[252:253], off
	s_barrier
	s_waitcnt lgkmcnt(0)
	v_mfma_f32_16x16x32_f16 v[14:17], v[198:201], v[230:233], v[14:17]
	v_mfma_f32_16x16x32_f16 v[22:25], v[198:201], v[238:241], v[22:25]
	v_mfma_f32_16x16x32_f16 v[34:37], v[206:209], v[230:233], v[34:37]
	v_mfma_f32_16x16x32_f16 v[46:49], v[206:209], v[238:241], v[46:49]
	v_mfma_f32_16x16x32_f16 v[58:61], v[214:217], v[230:233], v[58:61]
	v_mfma_f32_16x16x32_f16 v[70:73], v[214:217], v[238:241], v[70:73]
	v_mfma_f32_16x16x32_f16 v[78:81], v[222:225], v[230:233], v[78:81]
	v_mfma_f32_16x16x32_f16 v[86:89], v[222:225], v[238:241], v[86:89]
	v_mfma_f32_16x16x32_f16 v[14:17], v[202:205], v[234:237], v[14:17]
	v_mfma_f32_16x16x32_f16 v[22:25], v[202:205], v[242:245], v[22:25]
	v_mfma_f32_16x16x32_f16 v[34:37], v[210:213], v[234:237], v[34:37]
	v_mfma_f32_16x16x32_f16 v[46:49], v[210:213], v[242:245], v[46:49]
	v_mfma_f32_16x16x32_f16 v[58:61], v[218:221], v[234:237], v[58:61]
	v_mfma_f32_16x16x32_f16 v[70:73], v[218:221], v[242:245], v[70:73]
	v_mfma_f32_16x16x32_f16 v[78:81], v[226:229], v[234:237], v[78:81]
	v_mfma_f32_16x16x32_f16 v[86:89], v[226:229], v[242:245], v[86:89]
	v_lshl_add_u64 v[252:253], v[192:193], 0, s[26:27]
	s_mov_b32 m0, s69
	s_barrier
	ds_read_b128 v[198:201], v173 offset:16384
	ds_read_b128 v[202:205], v173 offset:17408
	ds_read_b128 v[206:209], v173 offset:18432
	ds_read_b128 v[210:213], v173 offset:19456
	ds_read_b128 v[214:217], v173 offset:20480
	ds_read_b128 v[218:221], v173 offset:21504
	ds_read_b128 v[222:225], v173 offset:22528
	ds_read_b128 v[226:229], v173 offset:23552
	global_load_lds_dwordx4 v[252:253], off
	s_mov_b32 m0, s70
	v_lshl_add_u64 v[252:253], v[246:247], 0, s[26:27]
	global_load_lds_dwordx4 v[252:253], off
	s_barrier
	s_waitcnt lgkmcnt(0)
	v_mfma_f32_16x16x32_f16 v[26:29], v[198:201], v[176:179], v[26:29]
	v_mfma_f32_16x16x32_f16 v[38:41], v[198:201], v[184:187], v[38:41]
	v_mfma_f32_16x16x32_f16 v[50:53], v[206:209], v[176:179], v[50:53]
	v_mfma_f32_16x16x32_f16 v[62:65], v[206:209], v[184:187], v[62:65]
	v_mfma_f32_16x16x32_f16 v[74:77], v[214:217], v[176:179], v[74:77]
	v_mfma_f32_16x16x32_f16 v[82:85], v[214:217], v[184:187], v[82:85]
	v_mfma_f32_16x16x32_f16 v[90:93], v[222:225], v[176:179], v[90:93]
	v_mfma_f32_16x16x32_f16 v[94:97], v[222:225], v[184:187], v[94:97]
	v_mfma_f32_16x16x32_f16 v[26:29], v[202:205], v[180:183], v[26:29]
	v_mfma_f32_16x16x32_f16 v[38:41], v[202:205], v[188:191], v[38:41]
	v_mfma_f32_16x16x32_f16 v[50:53], v[210:213], v[180:183], v[50:53]
	v_mfma_f32_16x16x32_f16 v[62:65], v[210:213], v[188:191], v[62:65]
	v_mfma_f32_16x16x32_f16 v[74:77], v[218:221], v[180:183], v[74:77]
	v_mfma_f32_16x16x32_f16 v[82:85], v[218:221], v[188:191], v[82:85]
	v_mfma_f32_16x16x32_f16 v[90:93], v[226:229], v[180:183], v[90:93]
	v_mfma_f32_16x16x32_f16 v[94:97], v[226:229], v[188:191], v[94:97]
	s_barrier
	v_lshl_add_u64 v[176:177], v[248:249], 0, s[28:29]
	s_mov_b32 m0, s71
	global_load_lds_dwordx4 v[176:177], off
	s_mov_b32 m0, s72
	v_lshl_add_u64 v[176:177], v[250:251], 0, s[28:29]
	global_load_lds_dwordx4 v[176:177], off
	s_waitcnt vmcnt(6)
	s_barrier
	v_mfma_f32_16x16x32_f16 v[98:101], v[198:201], v[230:233], v[98:101]
	v_mfma_f32_16x16x32_f16 v[102:105], v[198:201], v[238:241], v[102:105]
	v_mfma_f32_16x16x32_f16 v[106:109], v[206:209], v[230:233], v[106:109]
	v_mfma_f32_16x16x32_f16 v[110:113], v[206:209], v[238:241], v[110:113]
	v_mfma_f32_16x16x32_f16 v[114:117], v[214:217], v[230:233], v[114:117]
	v_mfma_f32_16x16x32_f16 v[118:121], v[214:217], v[238:241], v[118:121]
	v_mfma_f32_16x16x32_f16 v[122:125], v[222:225], v[230:233], v[122:125]
	v_mfma_f32_16x16x32_f16 v[126:129], v[222:225], v[238:241], v[126:129]
	v_mfma_f32_16x16x32_f16 v[98:101], v[202:205], v[234:237], v[98:101]
	v_mfma_f32_16x16x32_f16 v[102:105], v[202:205], v[242:245], v[102:105]
	v_mfma_f32_16x16x32_f16 v[106:109], v[210:213], v[234:237], v[106:109]
	v_mfma_f32_16x16x32_f16 v[110:113], v[210:213], v[242:245], v[110:113]
	v_mfma_f32_16x16x32_f16 v[114:117], v[218:221], v[234:237], v[114:117]
	v_mfma_f32_16x16x32_f16 v[118:121], v[218:221], v[242:245], v[118:121]
	v_mfma_f32_16x16x32_f16 v[122:125], v[226:229], v[234:237], v[122:125]
	v_mfma_f32_16x16x32_f16 v[126:129], v[226:229], v[242:245], v[126:129]
	s_barrier
	ds_read_b128 v[176:179], v144
	ds_read_b128 v[180:183], v145
	ds_read_b128 v[184:187], v150
	ds_read_b128 v[188:191], v151
	v_lshl_add_u64 v[230:231], v[192:193], 0, s[28:29]
	s_mov_b32 m0, s73
	ds_read_b128 v[198:201], v173 offset:32768
	ds_read_b128 v[202:205], v173 offset:33792
	ds_read_b128 v[206:209], v173 offset:34816
	ds_read_b128 v[210:213], v173 offset:35840
	ds_read_b128 v[214:217], v173 offset:36864
	ds_read_b128 v[218:221], v173 offset:37888
	ds_read_b128 v[222:225], v173 offset:38912
	ds_read_b128 v[226:229], v173 offset:39936
	global_load_lds_dwordx4 v[230:231], off
	s_mov_b32 m0, s74
	v_lshl_add_u64 v[230:231], v[246:247], 0, s[28:29]
	global_load_lds_dwordx4 v[230:231], off
	s_waitcnt lgkmcnt(8)
	s_barrier
	s_waitcnt lgkmcnt(0)
	v_mfma_f32_16x16x32_f16 v[2:5], v[198:201], v[176:179], v[2:5]
	v_mfma_f32_16x16x32_f16 v[6:9], v[198:201], v[184:187], v[6:9]
	v_mfma_f32_16x16x32_f16 v[10:13], v[206:209], v[176:179], v[10:13]
	v_mfma_f32_16x16x32_f16 v[18:21], v[206:209], v[184:187], v[18:21]
	v_mfma_f32_16x16x32_f16 v[30:33], v[214:217], v[176:179], v[30:33]
	v_mfma_f32_16x16x32_f16 v[42:45], v[214:217], v[184:187], v[42:45]
	v_mfma_f32_16x16x32_f16 v[54:57], v[222:225], v[176:179], v[54:57]
	v_mfma_f32_16x16x32_f16 v[66:69], v[222:225], v[184:187], v[66:69]
	v_mfma_f32_16x16x32_f16 v[2:5], v[202:205], v[180:183], v[2:5]
	v_mfma_f32_16x16x32_f16 v[6:9], v[202:205], v[188:191], v[6:9]
	v_mfma_f32_16x16x32_f16 v[10:13], v[210:213], v[180:183], v[10:13]
	v_mfma_f32_16x16x32_f16 v[18:21], v[210:213], v[188:191], v[18:21]
	v_mfma_f32_16x16x32_f16 v[30:33], v[218:221], v[180:183], v[30:33]
	v_mfma_f32_16x16x32_f16 v[42:45], v[218:221], v[188:191], v[42:45]
	v_mfma_f32_16x16x32_f16 v[54:57], v[226:229], v[180:183], v[54:57]
	v_mfma_f32_16x16x32_f16 v[66:69], v[226:229], v[188:191], v[66:69]
	s_barrier
	v_lshl_add_u64 v[252:253], v[248:249], 0, s[30:31]
	s_mov_b32 m0, s75
	ds_read_b128 v[230:233], v146
	ds_read_b128 v[234:237], v147
	ds_read_b128 v[238:241], v148
	ds_read_b128 v[242:245], v149
	global_load_lds_dwordx4 v[252:253], off
	s_mov_b32 m0, s76
	v_lshl_add_u64 v[252:253], v[250:251], 0, s[30:31]
	global_load_lds_dwordx4 v[252:253], off
	s_barrier
	s_waitcnt lgkmcnt(0)
	v_mfma_f32_16x16x32_f16 v[14:17], v[198:201], v[230:233], v[14:17]
	v_mfma_f32_16x16x32_f16 v[22:25], v[198:201], v[238:241], v[22:25]
	v_mfma_f32_16x16x32_f16 v[34:37], v[206:209], v[230:233], v[34:37]
	v_mfma_f32_16x16x32_f16 v[46:49], v[206:209], v[238:241], v[46:49]
	v_mfma_f32_16x16x32_f16 v[58:61], v[214:217], v[230:233], v[58:61]
	v_mfma_f32_16x16x32_f16 v[70:73], v[214:217], v[238:241], v[70:73]
	v_mfma_f32_16x16x32_f16 v[78:81], v[222:225], v[230:233], v[78:81]
	v_mfma_f32_16x16x32_f16 v[86:89], v[222:225], v[238:241], v[86:89]
	v_mfma_f32_16x16x32_f16 v[14:17], v[202:205], v[234:237], v[14:17]
	v_mfma_f32_16x16x32_f16 v[22:25], v[202:205], v[242:245], v[22:25]
	v_mfma_f32_16x16x32_f16 v[34:37], v[210:213], v[234:237], v[34:37]
	v_mfma_f32_16x16x32_f16 v[46:49], v[210:213], v[242:245], v[46:49]
	v_mfma_f32_16x16x32_f16 v[58:61], v[218:221], v[234:237], v[58:61]
	v_mfma_f32_16x16x32_f16 v[70:73], v[218:221], v[242:245], v[70:73]
	v_mfma_f32_16x16x32_f16 v[78:81], v[226:229], v[234:237], v[78:81]
	v_mfma_f32_16x16x32_f16 v[86:89], v[226:229], v[242:245], v[86:89]
	v_lshl_add_u64 v[192:193], v[192:193], 0, s[30:31]
	s_mov_b32 m0, s77
	s_barrier
	ds_read_b128 v[198:201], v173 offset:49152
	ds_read_b128 v[202:205], v173 offset:50176
	ds_read_b128 v[206:209], v173 offset:51200
	ds_read_b128 v[210:213], v173 offset:52224
	ds_read_b128 v[214:217], v173 offset:53248
	ds_read_b128 v[218:221], v173 offset:54272
	ds_read_b128 v[222:225], v173 offset:55296
	ds_read_b128 v[226:229], v173 offset:56320
	global_load_lds_dwordx4 v[192:193], off
	s_mov_b32 m0, s78
	v_lshl_add_u64 v[192:193], v[246:247], 0, s[30:31]
	global_load_lds_dwordx4 v[192:193], off
	s_barrier
	s_waitcnt lgkmcnt(0)
	v_mfma_f32_16x16x32_f16 v[26:29], v[198:201], v[176:179], v[26:29]
	v_mfma_f32_16x16x32_f16 v[38:41], v[198:201], v[184:187], v[38:41]
	v_mfma_f32_16x16x32_f16 v[50:53], v[206:209], v[176:179], v[50:53]
	v_mfma_f32_16x16x32_f16 v[62:65], v[206:209], v[184:187], v[62:65]
	v_mfma_f32_16x16x32_f16 v[74:77], v[214:217], v[176:179], v[74:77]
	v_mfma_f32_16x16x32_f16 v[82:85], v[214:217], v[184:187], v[82:85]
	v_mfma_f32_16x16x32_f16 v[90:93], v[222:225], v[176:179], v[90:93]
	v_mfma_f32_16x16x32_f16 v[94:97], v[222:225], v[184:187], v[94:97]
	v_mfma_f32_16x16x32_f16 v[26:29], v[202:205], v[180:183], v[26:29]
	v_mfma_f32_16x16x32_f16 v[38:41], v[202:205], v[188:191], v[38:41]
	v_mfma_f32_16x16x32_f16 v[50:53], v[210:213], v[180:183], v[50:53]
	v_mfma_f32_16x16x32_f16 v[62:65], v[210:213], v[188:191], v[62:65]
	v_mfma_f32_16x16x32_f16 v[74:77], v[218:221], v[180:183], v[74:77]
	v_mfma_f32_16x16x32_f16 v[82:85], v[218:221], v[188:191], v[82:85]
	v_mfma_f32_16x16x32_f16 v[90:93], v[226:229], v[180:183], v[90:93]
	v_mfma_f32_16x16x32_f16 v[94:97], v[226:229], v[188:191], v[94:97]
	s_barrier
	v_lshl_add_u64 v[176:177], v[248:249], 0, s[34:35]
	s_mov_b32 m0, s79
	global_load_lds_dwordx4 v[176:177], off
	s_mov_b32 m0, s80
	v_lshl_add_u64 v[176:177], v[250:251], 0, s[34:35]
	global_load_lds_dwordx4 v[176:177], off
	s_waitcnt vmcnt(6)
	s_barrier
	v_mfma_f32_16x16x32_f16 v[98:101], v[198:201], v[230:233], v[98:101]
	v_mfma_f32_16x16x32_f16 v[102:105], v[198:201], v[238:241], v[102:105]
	v_mfma_f32_16x16x32_f16 v[106:109], v[206:209], v[230:233], v[106:109]
	v_mfma_f32_16x16x32_f16 v[110:113], v[206:209], v[238:241], v[110:113]
	v_mfma_f32_16x16x32_f16 v[114:117], v[214:217], v[230:233], v[114:117]
	v_mfma_f32_16x16x32_f16 v[118:121], v[214:217], v[238:241], v[118:121]
	v_mfma_f32_16x16x32_f16 v[122:125], v[222:225], v[230:233], v[122:125]
	v_mfma_f32_16x16x32_f16 v[126:129], v[222:225], v[238:241], v[126:129]
	v_mfma_f32_16x16x32_f16 v[98:101], v[202:205], v[234:237], v[98:101]
	v_mfma_f32_16x16x32_f16 v[102:105], v[202:205], v[242:245], v[102:105]
	v_mfma_f32_16x16x32_f16 v[106:109], v[210:213], v[234:237], v[106:109]
	v_mfma_f32_16x16x32_f16 v[110:113], v[210:213], v[242:245], v[110:113]
	v_mfma_f32_16x16x32_f16 v[114:117], v[218:221], v[234:237], v[114:117]
	v_mfma_f32_16x16x32_f16 v[118:121], v[218:221], v[242:245], v[118:121]
	v_mfma_f32_16x16x32_f16 v[122:125], v[226:229], v[234:237], v[122:125]
	v_mfma_f32_16x16x32_f16 v[126:129], v[226:229], v[242:245], v[126:129]
	s_add_i32 s44, s44, 2
	s_add_u32 s42, s42, 0x100
	s_addc_u32 s43, s43, 0
	s_cmp_lt_u32 s44, 4
	s_barrier
	s_cbranch_scc1 .LBB9_38
	s_add_u32 s40, s40, 0x20380
	s_addc_u32 s41, s41, 0
	v_readfirstlane_b32 s39, v174
	v_lshl_add_u64 v[130:131], v[130:131], 1, s[40:41]
	s_mov_b32 m0, s39
	v_readfirstlane_b32 s39, v175
	ds_read_b128 v[134:137], v169
	ds_read_b128 v[138:141], v170
	ds_read_b128 v[152:155], v171
	ds_read_b128 v[156:159], v172
	ds_read_b128 v[166:169], v173
	ds_read_b128 v[176:179], v173 offset:1024
	ds_read_b128 v[180:183], v173 offset:2048
	ds_read_b128 v[184:187], v173 offset:3072
	ds_read_b128 v[188:191], v173 offset:4096
	ds_read_b128 v[198:201], v173 offset:5120
	ds_read_b128 v[202:205], v173 offset:6144
	ds_read_b128 v[206:209], v173 offset:7168
	global_load_lds_dwordx4 v[130:131], off
	s_mov_b32 m0, s39
	v_lshl_add_u64 v[130:131], v[132:133], 1, s[40:41]
	global_load_lds_dwordx4 v[130:131], off
	s_barrier
	s_waitcnt lgkmcnt(0)
	v_mfma_f32_16x16x32_f16 v[2:5], v[166:169], v[134:137], v[2:5]
	v_mfma_f32_16x16x32_f16 v[6:9], v[166:169], v[152:155], v[6:9]
	v_mfma_f32_16x16x32_f16 v[30:33], v[188:191], v[134:137], v[30:33]
	v_mfma_f32_16x16x32_f16 v[2:5], v[176:179], v[138:141], v[2:5]
	v_mfma_f32_16x16x32_f16 v[6:9], v[176:179], v[156:159], v[6:9]
	v_mfma_f32_16x16x32_f16 v[10:13], v[180:183], v[134:137], v[10:13]
	v_mfma_f32_16x16x32_f16 v[18:21], v[180:183], v[152:155], v[18:21]
	v_mfma_f32_16x16x32_f16 v[30:33], v[198:201], v[138:141], v[30:33]
	v_mfma_f32_16x16x32_f16 v[42:45], v[188:191], v[152:155], v[42:45]
	v_mfma_f32_16x16x32_f16 v[54:57], v[202:205], v[134:137], v[54:57]
	v_mfma_f32_16x16x32_f16 v[66:69], v[202:205], v[152:155], v[66:69]
	v_mfma_f32_16x16x32_f16 v[10:13], v[184:187], v[138:141], v[10:13]
	v_mfma_f32_16x16x32_f16 v[18:21], v[184:187], v[156:159], v[18:21]
	v_mfma_f32_16x16x32_f16 v[42:45], v[198:201], v[156:159], v[42:45]
	v_mfma_f32_16x16x32_f16 v[54:57], v[206:209], v[138:141], v[54:57]
	v_mfma_f32_16x16x32_f16 v[66:69], v[206:209], v[156:159], v[66:69]
	s_barrier
	ds_read_b128 v[130:133], v161
	ds_read_b128 v[210:213], v162
	ds_read_b128 v[160:163], v163
	ds_read_b128 v[214:217], v164
	s_barrier
	s_waitcnt lgkmcnt(0)
	v_mfma_f32_16x16x32_f16 v[58:61], v[188:191], v[130:133], v[58:61]
	v_mfma_f32_16x16x32_f16 v[14:17], v[166:169], v[130:133], v[14:17]
	v_mfma_f32_16x16x32_f16 v[22:25], v[166:169], v[160:163], v[22:25]
	v_mfma_f32_16x16x32_f16 v[164:167], v[198:201], v[210:213], v[58:61]
	v_mfma_f32_16x16x32_f16 v[58:61], v[188:191], v[160:163], v[70:73]
	v_mfma_f32_16x16x32_f16 v[46:49], v[180:183], v[160:163], v[46:49]
	v_mfma_f32_16x16x32_f16 v[168:171], v[198:201], v[214:217], v[58:61]
	v_mfma_f32_16x16x32_f16 v[58:61], v[202:205], v[130:133], v[78:81]
	v_mfma_f32_16x16x32_f16 v[14:17], v[176:179], v[210:213], v[14:17]
	v_mfma_f32_16x16x32_f16 v[34:37], v[180:183], v[130:133], v[34:37]
	v_mfma_f32_16x16x32_f16 v[46:49], v[184:187], v[214:217], v[46:49]
	v_mfma_f32_16x16x32_f16 v[78:81], v[206:209], v[210:213], v[58:61]
	v_mfma_f32_16x16x32_f16 v[58:61], v[202:205], v[160:163], v[86:89]
	v_mfma_f32_16x16x32_f16 v[22:25], v[176:179], v[214:217], v[22:25]
	v_mfma_f32_16x16x32_f16 v[34:37], v[184:187], v[210:213], v[34:37]
	v_mfma_f32_16x16x32_f16 v[86:89], v[206:209], v[214:217], v[58:61]
	s_barrier
	s_nop 2
	ds_read_b128 v[58:61], v173 offset:16384
	ds_read_b128 v[70:73], v173 offset:17408
	ds_read_b128 v[174:177], v173 offset:18432
	ds_read_b128 v[178:181], v173 offset:19456
	ds_read_b128 v[182:185], v173 offset:20480
	ds_read_b128 v[186:189], v173 offset:21504
	ds_read_b128 v[190:193], v173 offset:22528
	ds_read_b128 v[198:201], v173 offset:23552
	s_waitcnt vmcnt(4)
	s_barrier
	s_waitcnt lgkmcnt(0)
	v_mfma_f32_16x16x32_f16 v[26:29], v[58:61], v[134:137], v[26:29]
	v_mfma_f32_16x16x32_f16 v[26:29], v[70:73], v[138:141], v[26:29]
	v_mfma_f32_16x16x32_f16 v[38:41], v[58:61], v[152:155], v[38:41]
	v_mfma_f32_16x16x32_f16 v[50:53], v[174:177], v[134:137], v[50:53]
	v_mfma_f32_16x16x32_f16 v[62:65], v[174:177], v[152:155], v[62:65]
	v_mfma_f32_16x16x32_f16 v[74:77], v[182:185], v[134:137], v[74:77]
	v_mfma_f32_16x16x32_f16 v[82:85], v[182:185], v[152:155], v[82:85]
	v_mfma_f32_16x16x32_f16 v[90:93], v[190:193], v[134:137], v[90:93]
	v_mfma_f32_16x16x32_f16 v[94:97], v[190:193], v[152:155], v[94:97]
	v_mfma_f32_16x16x32_f16 v[38:41], v[70:73], v[156:159], v[38:41]
	v_mfma_f32_16x16x32_f16 v[50:53], v[178:181], v[138:141], v[50:53]
	v_mfma_f32_16x16x32_f16 v[62:65], v[178:181], v[156:159], v[62:65]
	v_mfma_f32_16x16x32_f16 v[74:77], v[186:189], v[138:141], v[74:77]
	v_mfma_f32_16x16x32_f16 v[82:85], v[186:189], v[156:159], v[82:85]
	v_mfma_f32_16x16x32_f16 v[90:93], v[198:201], v[138:141], v[90:93]
	v_mfma_f32_16x16x32_f16 v[94:97], v[198:201], v[156:159], v[94:97]
	v_mfma_f32_16x16x32_f16 v[98:101], v[58:61], v[130:133], v[98:101]
	v_mfma_f32_16x16x32_f16 v[58:61], v[58:61], v[160:163], v[102:105]
	v_mfma_f32_16x16x32_f16 v[102:105], v[70:73], v[214:217], v[58:61]
	v_mfma_f32_16x16x32_f16 v[58:61], v[174:177], v[130:133], v[106:109]
	v_mfma_f32_16x16x32_f16 v[106:109], v[178:181], v[210:213], v[58:61]
	v_mfma_f32_16x16x32_f16 v[58:61], v[174:177], v[160:163], v[110:113]
	v_mfma_f32_16x16x32_f16 v[202:205], v[178:181], v[214:217], v[58:61]
	v_mfma_f32_16x16x32_f16 v[58:61], v[182:185], v[130:133], v[114:117]
	v_mfma_f32_16x16x32_f16 v[206:209], v[186:189], v[210:213], v[58:61]
	v_mfma_f32_16x16x32_f16 v[58:61], v[182:185], v[160:163], v[118:121]
	v_mfma_f32_16x16x32_f16 v[218:221], v[186:189], v[214:217], v[58:61]
	v_mfma_f32_16x16x32_f16 v[58:61], v[190:193], v[130:133], v[122:125]
	v_mfma_f32_16x16x32_f16 v[98:101], v[70:73], v[210:213], v[98:101]
	v_mfma_f32_16x16x32_f16 v[210:213], v[198:201], v[210:213], v[58:61]
	v_mfma_f32_16x16x32_f16 v[58:61], v[190:193], v[160:163], v[126:129]
	v_mfma_f32_16x16x32_f16 v[198:201], v[198:201], v[214:217], v[58:61]
	s_barrier
	ds_read_b128 v[110:113], v144
	ds_read_b128 v[130:133], v145
	ds_read_b128 v[214:217], v150
	ds_read_b128 v[222:225], v151
	s_nop 0
	ds_read_b128 v[58:61], v173 offset:32768
	ds_read_b128 v[70:73], v173 offset:33792
	ds_read_b128 v[114:117], v173 offset:34816
	ds_read_b128 v[118:121], v173 offset:35840
	ds_read_b128 v[134:137], v173 offset:36864
	ds_read_b128 v[138:141], v173 offset:37888
	ds_read_b128 v[178:181], v173 offset:38912
	ds_read_b128 v[226:229], v173 offset:39936
	s_waitcnt vmcnt(2)
	s_barrier
	s_waitcnt lgkmcnt(0)
	v_mfma_f32_16x16x32_f16 v[2:5], v[58:61], v[110:113], v[2:5]
	v_mfma_f32_16x16x32_f16 v[190:193], v[70:73], v[130:133], v[2:5]
	v_mfma_f32_16x16x32_f16 v[2:5], v[58:61], v[214:217], v[6:9]
	v_mfma_f32_16x16x32_f16 v[158:161], v[70:73], v[222:225], v[2:5]
	v_mfma_f32_16x16x32_f16 v[2:5], v[114:117], v[110:113], v[10:13]
	v_mfma_f32_16x16x32_f16 v[186:189], v[118:121], v[130:133], v[2:5]
	v_mfma_f32_16x16x32_f16 v[2:5], v[114:117], v[214:217], v[18:21]
	v_mfma_f32_16x16x32_f16 v[154:157], v[118:121], v[222:225], v[2:5]
	v_mfma_f32_16x16x32_f16 v[2:5], v[134:137], v[110:113], v[30:33]
	v_mfma_f32_16x16x32_f16 v[182:185], v[138:141], v[130:133], v[2:5]
	v_mfma_f32_16x16x32_f16 v[2:5], v[134:137], v[214:217], v[42:45]
	v_mfma_f32_16x16x32_f16 v[150:153], v[138:141], v[222:225], v[2:5]
	v_mfma_f32_16x16x32_f16 v[2:5], v[178:181], v[110:113], v[54:57]
	v_mfma_f32_16x16x32_f16 v[174:177], v[226:229], v[130:133], v[2:5]
	v_mfma_f32_16x16x32_f16 v[2:5], v[178:181], v[214:217], v[66:69]
	v_mfma_f32_16x16x32_f16 v[142:145], v[226:229], v[222:225], v[2:5]
	s_barrier
	s_nop 4
	ds_read_b128 v[2:5], v146
	ds_read_b128 v[10:13], v147
	ds_read_b128 v[18:21], v148
	ds_read_b128 v[42:45], v149
	s_waitcnt vmcnt(0)
	s_barrier
	s_waitcnt lgkmcnt(0)
	v_mfma_f32_16x16x32_f16 v[6:9], v[58:61], v[2:5], v[14:17]
	v_mfma_f32_16x16x32_f16 v[126:129], v[70:73], v[10:13], v[6:9]
	v_mfma_f32_16x16x32_f16 v[6:9], v[58:61], v[18:21], v[22:25]
	v_mfma_f32_16x16x32_f16 v[70:73], v[70:73], v[42:45], v[6:9]
	v_mfma_f32_16x16x32_f16 v[6:9], v[114:117], v[2:5], v[34:37]
	v_mfma_f32_16x16x32_f16 v[122:125], v[118:121], v[10:13], v[6:9]
	v_mfma_f32_16x16x32_f16 v[6:9], v[114:117], v[18:21], v[46:49]
	v_mfma_f32_16x16x32_f16 v[58:61], v[118:121], v[42:45], v[6:9]
	v_mfma_f32_16x16x32_f16 v[6:9], v[134:137], v[2:5], v[164:167]
	v_mfma_f32_16x16x32_f16 v[118:121], v[138:141], v[10:13], v[6:9]
	v_mfma_f32_16x16x32_f16 v[6:9], v[134:137], v[18:21], v[168:171]
	v_mfma_f32_16x16x32_f16 v[46:49], v[138:141], v[42:45], v[6:9]
	v_mfma_f32_16x16x32_f16 v[6:9], v[178:181], v[2:5], v[78:81]
	v_mfma_f32_16x16x32_f16 v[114:117], v[226:229], v[10:13], v[6:9]
	v_mfma_f32_16x16x32_f16 v[6:9], v[178:181], v[18:21], v[86:89]
	v_mfma_f32_16x16x32_f16 v[30:33], v[226:229], v[42:45], v[6:9]
	s_barrier
	s_nop 4
	ds_read_b128 v[6:9], v173 offset:49152
	ds_read_b128 v[14:17], v173 offset:50176
	ds_read_b128 v[22:25], v173 offset:51200
	ds_read_b128 v[34:37], v173 offset:52224
	ds_read_b128 v[54:57], v173 offset:53248
	ds_read_b128 v[66:69], v173 offset:54272
	ds_read_b128 v[78:81], v173 offset:55296
	ds_read_b128 v[86:89], v173 offset:56320
	s_barrier
	s_waitcnt lgkmcnt(0)
	v_mfma_f32_16x16x32_f16 v[26:29], v[6:9], v[110:113], v[26:29]
	v_mfma_f32_16x16x32_f16 v[178:181], v[14:17], v[130:133], v[26:29]
	v_mfma_f32_16x16x32_f16 v[26:29], v[6:9], v[214:217], v[38:41]
	v_mfma_f32_16x16x32_f16 v[146:149], v[14:17], v[222:225], v[26:29]
	v_mfma_f32_16x16x32_f16 v[26:29], v[22:25], v[110:113], v[50:53]
	v_mfma_f32_16x16x32_f16 v[170:173], v[34:37], v[130:133], v[26:29]
	v_mfma_f32_16x16x32_f16 v[26:29], v[22:25], v[214:217], v[62:65]
	v_mfma_f32_16x16x32_f16 v[138:141], v[34:37], v[222:225], v[26:29]
	v_mfma_f32_16x16x32_f16 v[26:29], v[54:57], v[110:113], v[74:77]
	v_mfma_f32_16x16x32_f16 v[166:169], v[66:69], v[130:133], v[26:29]
	v_mfma_f32_16x16x32_f16 v[26:29], v[54:57], v[214:217], v[82:85]
	v_mfma_f32_16x16x32_f16 v[134:137], v[66:69], v[222:225], v[26:29]
	v_mfma_f32_16x16x32_f16 v[26:29], v[78:81], v[110:113], v[90:93]
	v_mfma_f32_16x16x32_f16 v[162:165], v[86:89], v[130:133], v[26:29]
	v_mfma_f32_16x16x32_f16 v[26:29], v[78:81], v[214:217], v[94:97]
	v_mfma_f32_16x16x32_f16 v[130:133], v[86:89], v[222:225], v[26:29]
	v_mfma_f32_16x16x32_f16 v[26:29], v[6:9], v[2:5], v[98:101]
	v_mfma_f32_16x16x32_f16 v[6:9], v[6:9], v[18:21], v[102:105]
	v_mfma_f32_16x16x32_f16 v[110:113], v[14:17], v[10:13], v[26:29]
	v_mfma_f32_16x16x32_f16 v[26:29], v[14:17], v[42:45], v[6:9]
	v_mfma_f32_16x16x32_f16 v[6:9], v[22:25], v[2:5], v[106:109]
	v_mfma_f32_16x16x32_f16 v[106:109], v[34:37], v[10:13], v[6:9]
	v_mfma_f32_16x16x32_f16 v[6:9], v[22:25], v[18:21], v[202:205]
	v_mfma_f32_16x16x32_f16 v[14:17], v[34:37], v[42:45], v[6:9]
	v_mfma_f32_16x16x32_f16 v[6:9], v[54:57], v[2:5], v[206:209]
	v_mfma_f32_16x16x32_f16 v[2:5], v[78:81], v[2:5], v[210:213]
	v_mfma_f32_16x16x32_f16 v[102:105], v[66:69], v[10:13], v[6:9]
	v_mfma_f32_16x16x32_f16 v[6:9], v[54:57], v[18:21], v[218:221]
	v_mfma_f32_16x16x32_f16 v[98:101], v[86:89], v[10:13], v[2:5]
	v_mfma_f32_16x16x32_f16 v[2:5], v[78:81], v[18:21], v[198:201]
	v_mfma_f32_16x16x32_f16 v[6:9], v[66:69], v[42:45], v[6:9]
	v_mfma_f32_16x16x32_f16 v[2:5], v[86:89], v[42:45], v[2:5]
	s_cmpk_gt_u32 s54, 0xff
	s_barrier
	s_cbranch_scc1 .LBB9_34
	s_barrier
	s_branch .LBB9_34

.LBB10_12:
	ds_read_b128 v[182:185], v171
	ds_read_b128 v[186:189], v173
	ds_read_b128 v[190:193], v174
	ds_read_b128 v[194:197], v175
	v_add_u32_e32 v177, 0xc000, v148
	v_lshl_add_u64 v[246:247], v[136:137], 0, s[44:45]
	v_add_u32_e32 v176, s63, v170
	v_lshl_add_u64 v[178:179], v[246:247], 0, s[28:29]
	s_mov_b32 m0, s70
	ds_read_b128 v[198:201], v176
	ds_read_b128 v[202:205], v176 offset:1024
	ds_read_b128 v[206:209], v176 offset:2048
	ds_read_b128 v[210:213], v176 offset:3072
	ds_read_b128 v[214:217], v176 offset:4096
	ds_read_b128 v[218:221], v176 offset:5120
	ds_read_b128 v[222:225], v176 offset:6144
	ds_read_b128 v[226:229], v176 offset:7168
	global_load_lds_dwordx4 v[178:179], off
	v_add_u32_e32 v178, 0xe000, v148
	v_lshl_add_u64 v[248:249], v[134:135], 0, s[44:45]
	s_mov_b32 m0, s71
	v_lshl_add_u64 v[230:231], v[248:249], 0, s[28:29]
	global_load_lds_dwordx4 v[230:231], off
	s_waitcnt lgkmcnt(8)
	s_barrier
	s_waitcnt lgkmcnt(0)
	v_mfma_f32_16x16x32_f16 v[126:129], v[198:201], v[182:185], v[126:129]
	v_mfma_f32_16x16x32_f16 v[122:125], v[198:201], v[190:193], v[122:125]
	v_mfma_f32_16x16x32_f16 v[118:121], v[206:209], v[182:185], v[118:121]
	v_mfma_f32_16x16x32_f16 v[114:117], v[206:209], v[190:193], v[114:117]
	v_mfma_f32_16x16x32_f16 v[110:113], v[214:217], v[182:185], v[110:113]
	v_mfma_f32_16x16x32_f16 v[106:109], v[214:217], v[190:193], v[106:109]
	v_mfma_f32_16x16x32_f16 v[102:105], v[222:225], v[182:185], v[102:105]
	v_mfma_f32_16x16x32_f16 v[98:101], v[222:225], v[190:193], v[98:101]
	v_mfma_f32_16x16x32_f16 v[126:129], v[202:205], v[186:189], v[126:129]
	v_mfma_f32_16x16x32_f16 v[122:125], v[202:205], v[194:197], v[122:125]
	v_mfma_f32_16x16x32_f16 v[118:121], v[210:213], v[186:189], v[118:121]
	v_mfma_f32_16x16x32_f16 v[114:117], v[210:213], v[194:197], v[114:117]
	v_mfma_f32_16x16x32_f16 v[110:113], v[218:221], v[186:189], v[110:113]
	v_mfma_f32_16x16x32_f16 v[106:109], v[218:221], v[194:197], v[106:109]
	v_mfma_f32_16x16x32_f16 v[102:105], v[226:229], v[186:189], v[102:105]
	v_mfma_f32_16x16x32_f16 v[98:101], v[226:229], v[194:197], v[98:101]
	s_barrier
	v_lshl_add_u64 v[250:251], v[140:141], 0, s[44:45]
	v_lshl_add_u64 v[252:253], v[250:251], 0, s[30:31]
	s_mov_b32 m0, s72
	ds_read_b128 v[230:233], v162
	ds_read_b128 v[234:237], v163
	ds_read_b128 v[238:241], v164
	ds_read_b128 v[242:245], v165
	global_load_lds_dwordx4 v[252:253], off
	v_lshl_add_u64 v[252:253], v[138:139], 0, s[44:45]
	s_mov_b32 m0, s73
	v_lshl_add_u64 v[254:255], v[252:253], 0, s[30:31]
	global_load_lds_dwordx4 v[254:255], off
	s_barrier
	s_waitcnt lgkmcnt(0)
	v_mfma_f32_16x16x32_f16 v[94:97], v[198:201], v[230:233], v[94:97]
	v_mfma_f32_16x16x32_f16 v[90:93], v[198:201], v[238:241], v[90:93]
	v_mfma_f32_16x16x32_f16 v[86:89], v[206:209], v[230:233], v[86:89]
	v_mfma_f32_16x16x32_f16 v[82:85], v[206:209], v[238:241], v[82:85]
	v_mfma_f32_16x16x32_f16 v[78:81], v[214:217], v[230:233], v[78:81]
	v_mfma_f32_16x16x32_f16 v[74:77], v[214:217], v[238:241], v[74:77]
	v_mfma_f32_16x16x32_f16 v[70:73], v[222:225], v[230:233], v[70:73]
	v_mfma_f32_16x16x32_f16 v[66:69], v[222:225], v[238:241], v[66:69]
	v_mfma_f32_16x16x32_f16 v[94:97], v[202:205], v[234:237], v[94:97]
	v_mfma_f32_16x16x32_f16 v[90:93], v[202:205], v[242:245], v[90:93]
	v_mfma_f32_16x16x32_f16 v[86:89], v[210:213], v[234:237], v[86:89]
	v_mfma_f32_16x16x32_f16 v[82:85], v[210:213], v[242:245], v[82:85]
	v_mfma_f32_16x16x32_f16 v[78:81], v[218:221], v[234:237], v[78:81]
	v_mfma_f32_16x16x32_f16 v[74:77], v[218:221], v[242:245], v[74:77]
	v_mfma_f32_16x16x32_f16 v[70:73], v[226:229], v[234:237], v[70:73]
	v_mfma_f32_16x16x32_f16 v[66:69], v[226:229], v[242:245], v[66:69]
	v_lshl_add_u64 v[254:255], v[246:247], 0, s[30:31]
	s_mov_b32 m0, s74
	s_barrier
	ds_read_b128 v[198:201], v176 offset:16384
	ds_read_b128 v[202:205], v176 offset:17408
	ds_read_b128 v[206:209], v176 offset:18432
	ds_read_b128 v[210:213], v176 offset:19456
	ds_read_b128 v[214:217], v176 offset:20480
	ds_read_b128 v[218:221], v176 offset:21504
	ds_read_b128 v[222:225], v176 offset:22528
	ds_read_b128 v[226:229], v176 offset:23552
	global_load_lds_dwordx4 v[254:255], off
	s_mov_b32 m0, s75
	v_lshl_add_u64 v[254:255], v[248:249], 0, s[30:31]
	global_load_lds_dwordx4 v[254:255], off
	s_barrier
	s_waitcnt lgkmcnt(0)
	v_mfma_f32_16x16x32_f16 v[62:65], v[198:201], v[182:185], v[62:65]
	v_mfma_f32_16x16x32_f16 v[58:61], v[198:201], v[190:193], v[58:61]
	v_mfma_f32_16x16x32_f16 v[54:57], v[206:209], v[182:185], v[54:57]
	v_mfma_f32_16x16x32_f16 v[50:53], v[206:209], v[190:193], v[50:53]
	v_mfma_f32_16x16x32_f16 v[46:49], v[214:217], v[182:185], v[46:49]
	v_mfma_f32_16x16x32_f16 v[42:45], v[214:217], v[190:193], v[42:45]
	v_mfma_f32_16x16x32_f16 v[38:41], v[222:225], v[182:185], v[38:41]
	v_mfma_f32_16x16x32_f16 v[34:37], v[222:225], v[190:193], v[34:37]
	v_mfma_f32_16x16x32_f16 v[62:65], v[202:205], v[186:189], v[62:65]
	v_mfma_f32_16x16x32_f16 v[58:61], v[202:205], v[194:197], v[58:61]
	v_mfma_f32_16x16x32_f16 v[54:57], v[210:213], v[186:189], v[54:57]
	v_mfma_f32_16x16x32_f16 v[50:53], v[210:213], v[194:197], v[50:53]
	v_mfma_f32_16x16x32_f16 v[46:49], v[218:221], v[186:189], v[46:49]
	v_mfma_f32_16x16x32_f16 v[42:45], v[218:221], v[194:197], v[42:45]
	v_mfma_f32_16x16x32_f16 v[38:41], v[226:229], v[186:189], v[38:41]
	v_mfma_f32_16x16x32_f16 v[34:37], v[226:229], v[194:197], v[34:37]
	s_barrier
	v_lshl_add_u64 v[182:183], v[250:251], 0, s[34:35]
	s_mov_b32 m0, s76
	global_load_lds_dwordx4 v[182:183], off
	s_mov_b32 m0, s77
	v_lshl_add_u64 v[182:183], v[252:253], 0, s[34:35]
	global_load_lds_dwordx4 v[182:183], off
	s_waitcnt vmcnt(6)
	s_barrier
	v_mfma_f32_16x16x32_f16 v[30:33], v[198:201], v[230:233], v[30:33]
	v_mfma_f32_16x16x32_f16 v[26:29], v[198:201], v[238:241], v[26:29]
	v_mfma_f32_16x16x32_f16 v[22:25], v[206:209], v[230:233], v[22:25]
	v_mfma_f32_16x16x32_f16 v[18:21], v[206:209], v[238:241], v[18:21]
	v_mfma_f32_16x16x32_f16 v[14:17], v[214:217], v[230:233], v[14:17]
	v_mfma_f32_16x16x32_f16 v[10:13], v[214:217], v[238:241], v[10:13]
	v_mfma_f32_16x16x32_f16 v[6:9], v[222:225], v[230:233], v[6:9]
	v_mfma_f32_16x16x32_f16 v[2:5], v[222:225], v[238:241], v[2:5]
	v_mfma_f32_16x16x32_f16 v[30:33], v[202:205], v[234:237], v[30:33]
	v_mfma_f32_16x16x32_f16 v[26:29], v[202:205], v[242:245], v[26:29]
	v_mfma_f32_16x16x32_f16 v[22:25], v[210:213], v[234:237], v[22:25]
	v_mfma_f32_16x16x32_f16 v[18:21], v[210:213], v[242:245], v[18:21]
	v_mfma_f32_16x16x32_f16 v[14:17], v[218:221], v[234:237], v[14:17]
	v_mfma_f32_16x16x32_f16 v[10:13], v[218:221], v[242:245], v[10:13]
	v_mfma_f32_16x16x32_f16 v[6:9], v[226:229], v[234:237], v[6:9]
	v_mfma_f32_16x16x32_f16 v[2:5], v[226:229], v[242:245], v[2:5]
	s_barrier
	ds_read_b128 v[182:185], v144
	ds_read_b128 v[186:189], v145
	ds_read_b128 v[190:193], v146
	ds_read_b128 v[194:197], v147
	v_lshl_add_u64 v[230:231], v[246:247], 0, s[34:35]
	s_mov_b32 m0, s78
	ds_read_b128 v[198:201], v176 offset:32768
	ds_read_b128 v[202:205], v176 offset:33792
	ds_read_b128 v[206:209], v176 offset:34816
	ds_read_b128 v[210:213], v176 offset:35840
	ds_read_b128 v[214:217], v176 offset:36864
	ds_read_b128 v[218:221], v176 offset:37888
	ds_read_b128 v[222:225], v176 offset:38912
	ds_read_b128 v[226:229], v176 offset:39936
	global_load_lds_dwordx4 v[230:231], off
	s_mov_b32 m0, s79
	v_lshl_add_u64 v[230:231], v[248:249], 0, s[34:35]
	global_load_lds_dwordx4 v[230:231], off
	s_waitcnt lgkmcnt(8)
	s_barrier
	s_waitcnt lgkmcnt(0)
	v_mfma_f32_16x16x32_f16 v[126:129], v[198:201], v[182:185], v[126:129]
	v_mfma_f32_16x16x32_f16 v[122:125], v[198:201], v[190:193], v[122:125]
	v_mfma_f32_16x16x32_f16 v[118:121], v[206:209], v[182:185], v[118:121]
	v_mfma_f32_16x16x32_f16 v[114:117], v[206:209], v[190:193], v[114:117]
	v_mfma_f32_16x16x32_f16 v[110:113], v[214:217], v[182:185], v[110:113]
	v_mfma_f32_16x16x32_f16 v[106:109], v[214:217], v[190:193], v[106:109]
	v_mfma_f32_16x16x32_f16 v[102:105], v[222:225], v[182:185], v[102:105]
	v_mfma_f32_16x16x32_f16 v[98:101], v[222:225], v[190:193], v[98:101]
	v_mfma_f32_16x16x32_f16 v[126:129], v[202:205], v[186:189], v[126:129]
	v_mfma_f32_16x16x32_f16 v[122:125], v[202:205], v[194:197], v[122:125]
	v_mfma_f32_16x16x32_f16 v[118:121], v[210:213], v[186:189], v[118:121]
	v_mfma_f32_16x16x32_f16 v[114:117], v[210:213], v[194:197], v[114:117]
	v_mfma_f32_16x16x32_f16 v[110:113], v[218:221], v[186:189], v[110:113]
	v_mfma_f32_16x16x32_f16 v[106:109], v[218:221], v[194:197], v[106:109]
	v_mfma_f32_16x16x32_f16 v[102:105], v[226:229], v[186:189], v[102:105]
	v_mfma_f32_16x16x32_f16 v[98:101], v[226:229], v[194:197], v[98:101]
	s_barrier
	v_lshl_add_u64 v[254:255], v[250:251], 0, s[36:37]
	s_mov_b32 m0, s80
	ds_read_b128 v[230:233], v150
	ds_read_b128 v[234:237], v151
	ds_read_b128 v[238:241], v152
	ds_read_b128 v[242:245], v153
	global_load_lds_dwordx4 v[254:255], off
	s_mov_b32 m0, s81
	v_lshl_add_u64 v[254:255], v[252:253], 0, s[36:37]
	global_load_lds_dwordx4 v[254:255], off
	s_barrier
	s_waitcnt lgkmcnt(0)
	v_mfma_f32_16x16x32_f16 v[94:97], v[198:201], v[230:233], v[94:97]
	v_mfma_f32_16x16x32_f16 v[90:93], v[198:201], v[238:241], v[90:93]
	v_mfma_f32_16x16x32_f16 v[86:89], v[206:209], v[230:233], v[86:89]
	v_mfma_f32_16x16x32_f16 v[82:85], v[206:209], v[238:241], v[82:85]
	v_mfma_f32_16x16x32_f16 v[78:81], v[214:217], v[230:233], v[78:81]
	v_mfma_f32_16x16x32_f16 v[74:77], v[214:217], v[238:241], v[74:77]
	v_mfma_f32_16x16x32_f16 v[70:73], v[222:225], v[230:233], v[70:73]
	v_mfma_f32_16x16x32_f16 v[66:69], v[222:225], v[238:241], v[66:69]
	v_mfma_f32_16x16x32_f16 v[94:97], v[202:205], v[234:237], v[94:97]
	v_mfma_f32_16x16x32_f16 v[90:93], v[202:205], v[242:245], v[90:93]
	v_mfma_f32_16x16x32_f16 v[86:89], v[210:213], v[234:237], v[86:89]
	v_mfma_f32_16x16x32_f16 v[82:85], v[210:213], v[242:245], v[82:85]
	v_mfma_f32_16x16x32_f16 v[78:81], v[218:221], v[234:237], v[78:81]
	v_mfma_f32_16x16x32_f16 v[74:77], v[218:221], v[242:245], v[74:77]
	v_mfma_f32_16x16x32_f16 v[70:73], v[226:229], v[234:237], v[70:73]
	v_mfma_f32_16x16x32_f16 v[66:69], v[226:229], v[242:245], v[66:69]
	v_lshl_add_u64 v[246:247], v[246:247], 0, s[36:37]
	s_mov_b32 m0, s82
	s_barrier
	ds_read_b128 v[198:201], v176 offset:49152
	ds_read_b128 v[202:205], v176 offset:50176
	ds_read_b128 v[206:209], v176 offset:51200
	ds_read_b128 v[210:213], v176 offset:52224
	ds_read_b128 v[214:217], v176 offset:53248
	ds_read_b128 v[218:221], v176 offset:54272
	ds_read_b128 v[222:225], v176 offset:55296
	ds_read_b128 v[226:229], v176 offset:56320
	global_load_lds_dwordx4 v[246:247], off
	s_mov_b32 m0, s83
	v_lshl_add_u64 v[246:247], v[248:249], 0, s[36:37]
	global_load_lds_dwordx4 v[246:247], off
	s_barrier
	s_waitcnt lgkmcnt(0)
	v_mfma_f32_16x16x32_f16 v[62:65], v[198:201], v[182:185], v[62:65]
	v_mfma_f32_16x16x32_f16 v[58:61], v[198:201], v[190:193], v[58:61]
	v_mfma_f32_16x16x32_f16 v[54:57], v[206:209], v[182:185], v[54:57]
	v_mfma_f32_16x16x32_f16 v[50:53], v[206:209], v[190:193], v[50:53]
	v_mfma_f32_16x16x32_f16 v[46:49], v[214:217], v[182:185], v[46:49]
	v_mfma_f32_16x16x32_f16 v[42:45], v[214:217], v[190:193], v[42:45]
	v_mfma_f32_16x16x32_f16 v[38:41], v[222:225], v[182:185], v[38:41]
	v_mfma_f32_16x16x32_f16 v[34:37], v[222:225], v[190:193], v[34:37]
	v_mfma_f32_16x16x32_f16 v[62:65], v[202:205], v[186:189], v[62:65]
	v_mfma_f32_16x16x32_f16 v[58:61], v[202:205], v[194:197], v[58:61]
	v_mfma_f32_16x16x32_f16 v[54:57], v[210:213], v[186:189], v[54:57]
	v_mfma_f32_16x16x32_f16 v[50:53], v[210:213], v[194:197], v[50:53]
	v_mfma_f32_16x16x32_f16 v[46:49], v[218:221], v[186:189], v[46:49]
	v_mfma_f32_16x16x32_f16 v[42:45], v[218:221], v[194:197], v[42:45]
	v_mfma_f32_16x16x32_f16 v[38:41], v[226:229], v[186:189], v[38:41]
	v_mfma_f32_16x16x32_f16 v[34:37], v[226:229], v[194:197], v[34:37]
	s_barrier
	v_lshl_add_u64 v[182:183], v[250:251], 0, s[38:39]
	s_mov_b32 m0, s84
	global_load_lds_dwordx4 v[182:183], off
	s_mov_b32 m0, s85
	v_lshl_add_u64 v[182:183], v[252:253], 0, s[38:39]
	global_load_lds_dwordx4 v[182:183], off
	s_waitcnt vmcnt(6)
	s_barrier
	v_mfma_f32_16x16x32_f16 v[30:33], v[198:201], v[230:233], v[30:33]
	v_mfma_f32_16x16x32_f16 v[26:29], v[198:201], v[238:241], v[26:29]
	v_mfma_f32_16x16x32_f16 v[22:25], v[206:209], v[230:233], v[22:25]
	v_mfma_f32_16x16x32_f16 v[18:21], v[206:209], v[238:241], v[18:21]
	v_mfma_f32_16x16x32_f16 v[14:17], v[214:217], v[230:233], v[14:17]
	v_mfma_f32_16x16x32_f16 v[10:13], v[214:217], v[238:241], v[10:13]
	v_mfma_f32_16x16x32_f16 v[6:9], v[222:225], v[230:233], v[6:9]
	v_mfma_f32_16x16x32_f16 v[2:5], v[222:225], v[238:241], v[2:5]
	v_mfma_f32_16x16x32_f16 v[30:33], v[202:205], v[234:237], v[30:33]
	v_mfma_f32_16x16x32_f16 v[26:29], v[202:205], v[242:245], v[26:29]
	v_mfma_f32_16x16x32_f16 v[22:25], v[210:213], v[234:237], v[22:25]
	v_mfma_f32_16x16x32_f16 v[18:21], v[210:213], v[242:245], v[18:21]
	v_mfma_f32_16x16x32_f16 v[14:17], v[218:221], v[234:237], v[14:17]
	v_mfma_f32_16x16x32_f16 v[10:13], v[218:221], v[242:245], v[10:13]
	v_mfma_f32_16x16x32_f16 v[6:9], v[226:229], v[234:237], v[6:9]
	v_mfma_f32_16x16x32_f16 v[2:5], v[226:229], v[242:245], v[2:5]
	s_add_i32 s46, s46, 2
	s_add_u32 s44, s44, 0x100
	s_addc_u32 s45, s45, 0
	s_cmp_lt_u32 s46, 28
	s_barrier
	s_cbranch_scc1 .LBB10_12
	s_add_u32 s42, s42, 0x80f80
	s_addc_u32 s43, s43, 0
	v_readfirstlane_b32 s44, v177
	v_lshl_add_u64 v[130:131], v[130:131], 1, s[42:43]
	s_mov_b32 m0, s44
	ds_read_b128 v[134:137], v171
	ds_read_b128 v[138:141], v173
	ds_read_b128 v[154:157], v174
	ds_read_b128 v[168:171], v175
	ds_read_b128 v[182:185], v176
	ds_read_b128 v[186:189], v176 offset:1024
	ds_read_b128 v[190:193], v176 offset:2048
	ds_read_b128 v[194:197], v176 offset:3072
	ds_read_b128 v[198:201], v176 offset:4096
	ds_read_b128 v[202:205], v176 offset:5120
	ds_read_b128 v[206:209], v176 offset:6144
	ds_read_b128 v[210:213], v176 offset:7168
	global_load_lds_dwordx4 v[130:131], off
	v_lshl_add_u64 v[130:131], v[132:133], 1, s[42:43]
	v_readfirstlane_b32 s42, v178
	s_mov_b32 m0, s42
	s_nop 0
	global_load_lds_dwordx4 v[130:131], off
	s_barrier
	s_waitcnt lgkmcnt(0)
	v_mfma_f32_16x16x32_f16 v[122:125], v[182:185], v[154:157], v[122:125]
	v_mfma_f32_16x16x32_f16 v[110:113], v[198:201], v[134:137], v[110:113]
	v_mfma_f32_16x16x32_f16 v[98:101], v[206:209], v[154:157], v[98:101]
	v_mfma_f32_16x16x32_f16 v[126:129], v[182:185], v[134:137], v[126:129]
	v_mfma_f32_16x16x32_f16 v[122:125], v[186:189], v[168:171], v[122:125]
	v_mfma_f32_16x16x32_f16 v[118:121], v[190:193], v[134:137], v[118:121]
	v_mfma_f32_16x16x32_f16 v[114:117], v[190:193], v[154:157], v[114:117]
	v_mfma_f32_16x16x32_f16 v[130:133], v[202:205], v[138:141], v[110:113]
	v_mfma_f32_16x16x32_f16 v[106:109], v[198:201], v[154:157], v[106:109]
	v_mfma_f32_16x16x32_f16 v[102:105], v[206:209], v[134:137], v[102:105]
	v_mfma_f32_16x16x32_f16 v[98:101], v[210:213], v[168:171], v[98:101]
	v_mfma_f32_16x16x32_f16 v[126:129], v[186:189], v[138:141], v[126:129]
	v_mfma_f32_16x16x32_f16 v[118:121], v[194:197], v[138:141], v[118:121]
	v_mfma_f32_16x16x32_f16 v[114:117], v[194:197], v[168:171], v[114:117]
	v_mfma_f32_16x16x32_f16 v[214:217], v[202:205], v[168:171], v[106:109]
	v_mfma_f32_16x16x32_f16 v[102:105], v[210:213], v[138:141], v[102:105]
	s_barrier
	ds_read_b128 v[106:109], v162
	ds_read_b128 v[110:113], v163
	ds_read_b128 v[160:163], v164
	ds_read_b128 v[218:221], v165
	s_barrier
	s_waitcnt lgkmcnt(0)
	v_mfma_f32_16x16x32_f16 v[82:85], v[190:193], v[160:163], v[82:85]
	v_mfma_f32_16x16x32_f16 v[78:81], v[198:201], v[106:109], v[78:81]
	v_mfma_f32_16x16x32_f16 v[74:77], v[198:201], v[160:163], v[74:77]
	v_mfma_f32_16x16x32_f16 v[70:73], v[206:209], v[106:109], v[70:73]
	v_mfma_f32_16x16x32_f16 v[66:69], v[206:209], v[160:163], v[66:69]
	v_mfma_f32_16x16x32_f16 v[94:97], v[182:185], v[106:109], v[94:97]
	v_mfma_f32_16x16x32_f16 v[90:93], v[182:185], v[160:163], v[90:93]
	v_mfma_f32_16x16x32_f16 v[86:89], v[190:193], v[106:109], v[86:89]
	v_mfma_f32_16x16x32_f16 v[82:85], v[194:197], v[218:221], v[82:85]
	v_mfma_f32_16x16x32_f16 v[78:81], v[202:205], v[110:113], v[78:81]
	v_mfma_f32_16x16x32_f16 v[74:77], v[202:205], v[218:221], v[74:77]
	v_mfma_f32_16x16x32_f16 v[70:73], v[210:213], v[110:113], v[70:73]
	v_mfma_f32_16x16x32_f16 v[66:69], v[210:213], v[218:221], v[66:69]
	v_mfma_f32_16x16x32_f16 v[222:225], v[186:189], v[110:113], v[94:97]
	v_mfma_f32_16x16x32_f16 v[182:185], v[186:189], v[218:221], v[90:93]
	v_mfma_f32_16x16x32_f16 v[86:89], v[194:197], v[110:113], v[86:89]
	s_barrier
	ds_read_b128 v[90:93], v176 offset:16384
	ds_read_b128 v[94:97], v176 offset:17408
	ds_read_b128 v[186:189], v176 offset:18432
	ds_read_b128 v[190:193], v176 offset:19456
	ds_read_b128 v[194:197], v176 offset:20480
	ds_read_b128 v[198:201], v176 offset:21504
	ds_read_b128 v[202:205], v176 offset:22528
	ds_read_b128 v[206:209], v176 offset:23552
	s_waitcnt vmcnt(4)
	s_barrier
	s_waitcnt lgkmcnt(0)
	v_mfma_f32_16x16x32_f16 v[46:49], v[194:197], v[134:137], v[46:49]
	v_mfma_f32_16x16x32_f16 v[42:45], v[194:197], v[154:157], v[42:45]
	v_mfma_f32_16x16x32_f16 v[38:41], v[202:205], v[134:137], v[38:41]
	v_mfma_f32_16x16x32_f16 v[34:37], v[202:205], v[154:157], v[34:37]
	v_mfma_f32_16x16x32_f16 v[62:65], v[90:93], v[134:137], v[62:65]
	v_mfma_f32_16x16x32_f16 v[58:61], v[90:93], v[154:157], v[58:61]
	v_mfma_f32_16x16x32_f16 v[54:57], v[186:189], v[134:137], v[54:57]
	v_mfma_f32_16x16x32_f16 v[50:53], v[186:189], v[154:157], v[50:53]
	v_mfma_f32_16x16x32_f16 v[46:49], v[198:201], v[138:141], v[46:49]
	v_mfma_f32_16x16x32_f16 v[42:45], v[198:201], v[168:171], v[42:45]
	v_mfma_f32_16x16x32_f16 v[38:41], v[206:209], v[138:141], v[38:41]
	v_mfma_f32_16x16x32_f16 v[34:37], v[206:209], v[168:171], v[34:37]
	v_mfma_f32_16x16x32_f16 v[210:213], v[94:97], v[138:141], v[62:65]
	v_mfma_f32_16x16x32_f16 v[226:229], v[94:97], v[168:171], v[58:61]
	v_mfma_f32_16x16x32_f16 v[230:233], v[190:193], v[138:141], v[54:57]
	v_mfma_f32_16x16x32_f16 v[234:237], v[190:193], v[168:171], v[50:53]
	v_mfma_f32_16x16x32_f16 v[2:5], v[202:205], v[160:163], v[2:5]
	v_mfma_f32_16x16x32_f16 v[30:33], v[90:93], v[106:109], v[30:33]
	v_mfma_f32_16x16x32_f16 v[26:29], v[90:93], v[160:163], v[26:29]
	v_mfma_f32_16x16x32_f16 v[22:25], v[186:189], v[106:109], v[22:25]
	v_mfma_f32_16x16x32_f16 v[18:21], v[186:189], v[160:163], v[18:21]
	v_mfma_f32_16x16x32_f16 v[14:17], v[194:197], v[106:109], v[14:17]
	v_mfma_f32_16x16x32_f16 v[10:13], v[194:197], v[160:163], v[10:13]
	v_mfma_f32_16x16x32_f16 v[6:9], v[202:205], v[106:109], v[6:9]
	v_mfma_f32_16x16x32_f16 v[2:5], v[206:209], v[218:221], v[2:5]
	v_mfma_f32_16x16x32_f16 v[138:141], v[94:97], v[110:113], v[30:33]
	v_mfma_f32_16x16x32_f16 v[168:171], v[94:97], v[218:221], v[26:29]
	v_mfma_f32_16x16x32_f16 v[238:241], v[190:193], v[110:113], v[22:25]
	v_mfma_f32_16x16x32_f16 v[186:189], v[190:193], v[218:221], v[18:21]
	v_mfma_f32_16x16x32_f16 v[190:193], v[198:201], v[110:113], v[14:17]
	v_mfma_f32_16x16x32_f16 v[194:197], v[198:201], v[218:221], v[10:13]
	v_mfma_f32_16x16x32_f16 v[198:201], v[206:209], v[110:113], v[6:9]
	s_barrier
	s_nop 0
	ds_read_b128 v[6:9], v144
	ds_read_b128 v[10:13], v145
	ds_read_b128 v[14:17], v146
	ds_read_b128 v[160:163], v147
	ds_read_b128 v[18:21], v176 offset:32768
	ds_read_b128 v[22:25], v176 offset:33792
	ds_read_b128 v[26:29], v176 offset:34816
	ds_read_b128 v[50:53], v176 offset:35840
	ds_read_b128 v[202:205], v176 offset:36864
	ds_read_b128 v[206:209], v176 offset:37888
	ds_read_b128 v[218:221], v176 offset:38912
	ds_read_b128 v[242:245], v176 offset:39936
	s_waitcnt vmcnt(2)
	s_barrier
	s_waitcnt lgkmcnt(0)
	v_mfma_f32_16x16x32_f16 v[30:33], v[18:21], v[6:9], v[126:129]
	v_mfma_f32_16x16x32_f16 v[154:157], v[22:25], v[10:13], v[30:33]
	v_mfma_f32_16x16x32_f16 v[30:33], v[18:21], v[14:17], v[122:125]
	v_mfma_f32_16x16x32_f16 v[110:113], v[22:25], v[160:163], v[30:33]
	v_mfma_f32_16x16x32_f16 v[30:33], v[26:29], v[6:9], v[118:121]
	v_mfma_f32_16x16x32_f16 v[146:149], v[50:53], v[10:13], v[30:33]
	v_mfma_f32_16x16x32_f16 v[30:33], v[26:29], v[14:17], v[114:117]
	v_mfma_f32_16x16x32_f16 v[106:109], v[50:53], v[160:163], v[30:33]
	v_mfma_f32_16x16x32_f16 v[30:33], v[202:205], v[6:9], v[130:133]
	v_mfma_f32_16x16x32_f16 v[142:145], v[206:209], v[10:13], v[30:33]
	v_mfma_f32_16x16x32_f16 v[30:33], v[202:205], v[14:17], v[214:217]
	v_mfma_f32_16x16x32_f16 v[94:97], v[206:209], v[160:163], v[30:33]
	v_mfma_f32_16x16x32_f16 v[30:33], v[218:221], v[6:9], v[102:105]
	v_mfma_f32_16x16x32_f16 v[134:137], v[242:245], v[10:13], v[30:33]
	v_mfma_f32_16x16x32_f16 v[30:33], v[218:221], v[14:17], v[98:101]
	v_mfma_f32_16x16x32_f16 v[90:93], v[242:245], v[160:163], v[30:33]
	s_barrier
	ds_read_b128 v[102:105], v150
	ds_read_b128 v[114:117], v151
	ds_read_b128 v[118:121], v152
	ds_read_b128 v[126:129], v153
	s_waitcnt vmcnt(0)
	s_barrier
	s_waitcnt lgkmcnt(0)
	v_mfma_f32_16x16x32_f16 v[30:33], v[18:21], v[102:105], v[222:225]
	v_mfma_f32_16x16x32_f16 v[18:21], v[18:21], v[118:121], v[182:185]
	v_mfma_f32_16x16x32_f16 v[62:65], v[22:25], v[114:117], v[30:33]
	v_mfma_f32_16x16x32_f16 v[30:33], v[22:25], v[126:129], v[18:21]
	v_mfma_f32_16x16x32_f16 v[18:21], v[26:29], v[102:105], v[86:89]
	v_mfma_f32_16x16x32_f16 v[58:61], v[50:53], v[114:117], v[18:21]
	v_mfma_f32_16x16x32_f16 v[18:21], v[26:29], v[118:121], v[82:85]
	v_mfma_f32_16x16x32_f16 v[26:29], v[50:53], v[126:129], v[18:21]
	v_mfma_f32_16x16x32_f16 v[18:21], v[202:205], v[102:105], v[78:81]
	v_mfma_f32_16x16x32_f16 v[54:57], v[206:209], v[114:117], v[18:21]
	v_mfma_f32_16x16x32_f16 v[18:21], v[202:205], v[118:121], v[74:77]
	v_mfma_f32_16x16x32_f16 v[22:25], v[206:209], v[126:129], v[18:21]
	v_mfma_f32_16x16x32_f16 v[18:21], v[218:221], v[102:105], v[70:73]
	v_mfma_f32_16x16x32_f16 v[50:53], v[242:245], v[114:117], v[18:21]
	v_mfma_f32_16x16x32_f16 v[18:21], v[218:221], v[118:121], v[66:69]
	v_mfma_f32_16x16x32_f16 v[18:21], v[242:245], v[126:129], v[18:21]
	s_barrier
	ds_read_b128 v[86:89], v176 offset:49152
	ds_read_b128 v[150:153], v176 offset:50176
	ds_read_b128 v[182:185], v176 offset:51200
	ds_read_b128 v[202:205], v176 offset:52224
	ds_read_b128 v[206:209], v176 offset:53248
	ds_read_b128 v[214:217], v176 offset:54272
	ds_read_b128 v[218:221], v176 offset:55296
	ds_read_b128 v[174:177], v176 offset:56320
	s_barrier
	s_waitcnt lgkmcnt(0)
	v_mfma_f32_16x16x32_f16 v[66:69], v[86:89], v[6:9], v[210:213]
	v_mfma_f32_16x16x32_f16 v[130:133], v[150:153], v[10:13], v[66:69]
	v_mfma_f32_16x16x32_f16 v[66:69], v[86:89], v[14:17], v[226:229]
	v_mfma_f32_16x16x32_f16 v[78:81], v[150:153], v[160:163], v[66:69]
	v_mfma_f32_16x16x32_f16 v[66:69], v[182:185], v[6:9], v[230:233]
	v_mfma_f32_16x16x32_f16 v[46:49], v[206:209], v[6:9], v[46:49]
	v_mfma_f32_16x16x32_f16 v[6:9], v[218:221], v[6:9], v[38:41]
	v_mfma_f32_16x16x32_f16 v[122:125], v[202:205], v[10:13], v[66:69]
	v_mfma_f32_16x16x32_f16 v[66:69], v[182:185], v[14:17], v[234:237]
	v_mfma_f32_16x16x32_f16 v[42:45], v[206:209], v[14:17], v[42:45]
	v_mfma_f32_16x16x32_f16 v[82:85], v[174:177], v[10:13], v[6:9]
	v_mfma_f32_16x16x32_f16 v[6:9], v[218:221], v[14:17], v[34:37]
	v_mfma_f32_16x16x32_f16 v[74:77], v[202:205], v[160:163], v[66:69]
	v_mfma_f32_16x16x32_f16 v[98:101], v[214:217], v[10:13], v[46:49]
	v_mfma_f32_16x16x32_f16 v[70:73], v[214:217], v[160:163], v[42:45]
	v_mfma_f32_16x16x32_f16 v[66:69], v[174:177], v[160:163], v[6:9]
	v_mfma_f32_16x16x32_f16 v[6:9], v[86:89], v[102:105], v[138:141]
	v_mfma_f32_16x16x32_f16 v[46:49], v[150:153], v[114:117], v[6:9]
	v_mfma_f32_16x16x32_f16 v[6:9], v[86:89], v[118:121], v[168:171]
	v_mfma_f32_16x16x32_f16 v[14:17], v[150:153], v[126:129], v[6:9]
	v_mfma_f32_16x16x32_f16 v[6:9], v[182:185], v[102:105], v[238:241]
	v_mfma_f32_16x16x32_f16 v[42:45], v[202:205], v[114:117], v[6:9]
	v_mfma_f32_16x16x32_f16 v[6:9], v[182:185], v[118:121], v[186:189]
	v_mfma_f32_16x16x32_f16 v[10:13], v[202:205], v[126:129], v[6:9]
	v_mfma_f32_16x16x32_f16 v[6:9], v[206:209], v[102:105], v[190:193]
	v_mfma_f32_16x16x32_f16 v[38:41], v[214:217], v[114:117], v[6:9]
	v_mfma_f32_16x16x32_f16 v[6:9], v[206:209], v[118:121], v[194:197]
	v_mfma_f32_16x16x32_f16 v[34:37], v[218:221], v[102:105], v[198:201]
	v_mfma_f32_16x16x32_f16 v[2:5], v[218:221], v[118:121], v[2:5]
	v_mfma_f32_16x16x32_f16 v[6:9], v[214:217], v[126:129], v[6:9]
	v_mfma_f32_16x16x32_f16 v[34:37], v[174:177], v[114:117], v[34:37]
	v_mfma_f32_16x16x32_f16 v[2:5], v[174:177], v[126:129], v[2:5]
	s_cmpk_gt_u32 s61, 0xff
	s_barrier
	s_cbranch_scc1 .LBB10_15
	s_barrier
